# v99 + lever 1 (waitcnt cleanup): the redundant s_waitcnt lgkmcnt(0) after the barrier removed in the bf16 GEMM K-loops (32 sites; the same wait already precedes the barrier)
# speedup vs baseline: 1.0100x; 1.0001x over previous
.LBB0_189:
	s_add_i32 s38, s2, 2
	s_add_u32 s39, s74, 0xfffc0080
	s_addc_u32 s3, s75, -1
	s_cmp_eq_u32 s80, s2
	s_cselect_b32 s3, s47, s3
	s_cselect_b32 s2, s49, s39
	s_cselect_b32 s91, s86, s23
	s_cselect_b32 s90, s87, s22
	s_add_i32 s39, 0, 0x10000
	s_add_i32 s92, 0, 0x14000
	v_add_u32_e32 v148, s39, v133
	v_add_u32_e32 v166, s92, v133
	ds_read_b128 v[136:139], v148
	ds_read_b128 v[140:143], v148 offset:1024
	ds_read_b128 v[144:147], v148 offset:2048
	ds_read_b128 v[148:151], v148 offset:3072
	ds_read_b128 v[152:155], v166
	ds_read_b128 v[156:159], v166 offset:1024
	ds_read_b128 v[162:165], v166 offset:2048
	ds_read_b128 v[166:169], v166 offset:3072
	v_lshl_add_u64 v[202:203], s[74:75], 0, v[130:131]
	s_add_i32 m0, s33, 0xc000
	ds_read_b128 v[170:173], v135
	ds_read_b128 v[174:177], v135 offset:1024
	ds_read_b128 v[178:181], v135 offset:2048
	ds_read_b128 v[182:185], v135 offset:3072
	ds_read_b128 v[186:189], v135 offset:4096
	ds_read_b128 v[190:193], v135 offset:5120
	ds_read_b128 v[194:197], v135 offset:6144
	ds_read_b128 v[198:201], v135 offset:7168
	global_load_lds_dwordx4 v[202:203], off
	v_lshl_add_u64 v[202:203], v[202:203], 0, s[14:15]
	s_add_i32 m0, s33, 0xe000
	s_nop 0
	global_load_lds_dwordx4 v[202:203], off
	s_waitcnt vmcnt(8)
	s_waitcnt lgkmcnt(0)
	s_barrier
	s_setprio 1
	v_mfma_f32_16x16x32_bf16 v[124:127], v[136:139], v[170:173], v[124:127]
	v_mfma_f32_16x16x32_bf16 v[120:123], v[144:147], v[170:173], v[120:123]
	v_mfma_f32_16x16x32_bf16 v[108:111], v[136:139], v[178:181], v[108:111]
	v_mfma_f32_16x16x32_bf16 v[104:107], v[144:147], v[178:181], v[104:107]
	v_mfma_f32_16x16x32_bf16 v[92:95], v[136:139], v[186:189], v[92:95]
	v_mfma_f32_16x16x32_bf16 v[88:91], v[144:147], v[186:189], v[88:91]
	v_mfma_f32_16x16x32_bf16 v[76:79], v[136:139], v[194:197], v[76:79]
	v_mfma_f32_16x16x32_bf16 v[72:75], v[144:147], v[194:197], v[72:75]
	v_mfma_f32_16x16x32_bf16 v[124:127], v[140:143], v[174:177], v[124:127]
	v_mfma_f32_16x16x32_bf16 v[120:123], v[148:151], v[174:177], v[120:123]
	v_mfma_f32_16x16x32_bf16 v[108:111], v[140:143], v[182:185], v[108:111]
	v_mfma_f32_16x16x32_bf16 v[104:107], v[148:151], v[182:185], v[104:107]
	v_mfma_f32_16x16x32_bf16 v[92:95], v[140:143], v[190:193], v[92:95]
	v_mfma_f32_16x16x32_bf16 v[88:91], v[148:151], v[190:193], v[88:91]
	v_mfma_f32_16x16x32_bf16 v[76:79], v[140:143], v[198:201], v[76:79]
	v_mfma_f32_16x16x32_bf16 v[72:75], v[148:151], v[198:201], v[72:75]
	v_mfma_f32_16x16x32_bf16 v[116:119], v[152:155], v[170:173], v[116:119]
	v_mfma_f32_16x16x32_bf16 v[112:115], v[162:165], v[170:173], v[112:115]
	v_mfma_f32_16x16x32_bf16 v[100:103], v[152:155], v[178:181], v[100:103]
	v_mfma_f32_16x16x32_bf16 v[96:99], v[162:165], v[178:181], v[96:99]
	v_mfma_f32_16x16x32_bf16 v[84:87], v[152:155], v[186:189], v[84:87]
	v_mfma_f32_16x16x32_bf16 v[80:83], v[162:165], v[186:189], v[80:83]
	v_mfma_f32_16x16x32_bf16 v[68:71], v[152:155], v[194:197], v[68:71]
	v_mfma_f32_16x16x32_bf16 v[64:67], v[162:165], v[194:197], v[64:67]
	v_mfma_f32_16x16x32_bf16 v[116:119], v[156:159], v[174:177], v[116:119]
	v_mfma_f32_16x16x32_bf16 v[112:115], v[166:169], v[174:177], v[112:115]
	v_mfma_f32_16x16x32_bf16 v[100:103], v[156:159], v[182:185], v[100:103]
	v_mfma_f32_16x16x32_bf16 v[96:99], v[166:169], v[182:185], v[96:99]
	v_mfma_f32_16x16x32_bf16 v[84:87], v[156:159], v[190:193], v[84:87]
	v_mfma_f32_16x16x32_bf16 v[80:83], v[166:169], v[190:193], v[80:83]
	v_mfma_f32_16x16x32_bf16 v[68:71], v[156:159], v[198:201], v[68:71]
	v_mfma_f32_16x16x32_bf16 v[64:67], v[166:169], v[198:201], v[64:67]
	s_setprio 0
	s_barrier
	s_add_i32 s39, s39, s31
	v_lshl_add_u64 v[202:203], s[90:91], 0, v[160:161]
	s_mov_b32 m0, s39
	ds_read_b128 v[170:173], v135 offset:16384
	ds_read_b128 v[174:177], v135 offset:17408
	ds_read_b128 v[178:181], v135 offset:18432
	ds_read_b128 v[182:185], v135 offset:19456
	ds_read_b128 v[186:189], v135 offset:20480
	ds_read_b128 v[190:193], v135 offset:21504
	ds_read_b128 v[194:197], v135 offset:22528
	ds_read_b128 v[198:201], v135 offset:23552
	global_load_lds_dwordx4 v[202:203], off
	v_lshl_add_u64 v[204:205], v[202:203], 0, s[14:15]
	s_add_i32 m0, s39, 0x2000
	s_add_i32 s39, s92, s31
	global_load_lds_dwordx4 v[204:205], off
	v_lshl_add_u64 v[204:205], v[202:203], 0, s[60:61]
	s_mov_b32 m0, s39
	s_nop 0
	global_load_lds_dwordx4 v[204:205], off
	v_lshl_add_u64 v[204:205], v[202:203], 0, s[52:53]
	s_add_i32 m0, s39, 0x2000
	s_nop 0
	global_load_lds_dwordx4 v[204:205], off
	v_lshl_add_u64 v[204:205], s[2:3], 0, v[128:129]
	s_mov_b32 m0, s33
	v_lshl_add_u64 v[206:207], v[204:205], 0, s[14:15]
	global_load_lds_dwordx4 v[204:205], off
	s_mov_b32 m0, s58
	s_nop 0
	global_load_lds_dwordx4 v[206:207], off
	s_waitcnt vmcnt(8)
	s_waitcnt lgkmcnt(0)
	s_barrier
	s_setprio 1
	v_mfma_f32_16x16x32_bf16 v[60:63], v[136:139], v[170:173], v[60:63]
	v_mfma_f32_16x16x32_bf16 v[56:59], v[144:147], v[170:173], v[56:59]
	v_mfma_f32_16x16x32_bf16 v[44:47], v[136:139], v[178:181], v[44:47]
	v_mfma_f32_16x16x32_bf16 v[40:43], v[144:147], v[178:181], v[40:43]
	v_mfma_f32_16x16x32_bf16 v[28:31], v[136:139], v[186:189], v[28:31]
	v_mfma_f32_16x16x32_bf16 v[24:27], v[144:147], v[186:189], v[24:27]
	v_mfma_f32_16x16x32_bf16 v[12:15], v[136:139], v[194:197], v[12:15]
	v_mfma_f32_16x16x32_bf16 v[8:11], v[144:147], v[194:197], v[8:11]
	v_mfma_f32_16x16x32_bf16 v[60:63], v[140:143], v[174:177], v[60:63]
	v_mfma_f32_16x16x32_bf16 v[56:59], v[148:151], v[174:177], v[56:59]
	v_mfma_f32_16x16x32_bf16 v[44:47], v[140:143], v[182:185], v[44:47]
	v_mfma_f32_16x16x32_bf16 v[40:43], v[148:151], v[182:185], v[40:43]
	v_mfma_f32_16x16x32_bf16 v[28:31], v[140:143], v[190:193], v[28:31]
	v_mfma_f32_16x16x32_bf16 v[24:27], v[148:151], v[190:193], v[24:27]
	v_mfma_f32_16x16x32_bf16 v[12:15], v[140:143], v[198:201], v[12:15]
	v_mfma_f32_16x16x32_bf16 v[8:11], v[148:151], v[198:201], v[8:11]
	v_mfma_f32_16x16x32_bf16 v[52:55], v[152:155], v[170:173], v[52:55]
	v_mfma_f32_16x16x32_bf16 v[48:51], v[162:165], v[170:173], v[48:51]
	v_mfma_f32_16x16x32_bf16 v[36:39], v[152:155], v[178:181], v[36:39]
	v_mfma_f32_16x16x32_bf16 v[32:35], v[162:165], v[178:181], v[32:35]
	v_mfma_f32_16x16x32_bf16 v[20:23], v[152:155], v[186:189], v[20:23]
	v_mfma_f32_16x16x32_bf16 v[16:19], v[162:165], v[186:189], v[16:19]
	v_mfma_f32_16x16x32_bf16 v[4:7], v[152:155], v[194:197], v[4:7]
	v_mfma_f32_16x16x32_bf16 v[0:3], v[162:165], v[194:197], v[0:3]
	v_mfma_f32_16x16x32_bf16 v[52:55], v[156:159], v[174:177], v[52:55]
	v_mfma_f32_16x16x32_bf16 v[48:51], v[166:169], v[174:177], v[48:51]
	v_mfma_f32_16x16x32_bf16 v[36:39], v[156:159], v[182:185], v[36:39]
	v_mfma_f32_16x16x32_bf16 v[32:35], v[166:169], v[182:185], v[32:35]
	v_mfma_f32_16x16x32_bf16 v[20:23], v[156:159], v[190:193], v[20:23]
	v_mfma_f32_16x16x32_bf16 v[16:19], v[166:169], v[190:193], v[16:19]
	v_mfma_f32_16x16x32_bf16 v[4:7], v[156:159], v[198:201], v[4:7]
	v_mfma_f32_16x16x32_bf16 v[0:3], v[166:169], v[198:201], v[0:3]
	s_setprio 0
	s_barrier
	s_add_i32 s2, 0, 0x18000
	s_add_i32 s3, 0, 0x1c000
	v_add_u32_e32 v148, s2, v133
	v_add_u32_e32 v166, s3, v133
	ds_read_b128 v[136:139], v148
	ds_read_b128 v[140:143], v148 offset:1024
	ds_read_b128 v[144:147], v148 offset:2048
	ds_read_b128 v[148:151], v148 offset:3072
	ds_read_b128 v[152:155], v166
	ds_read_b128 v[156:159], v166 offset:1024
	ds_read_b128 v[162:165], v166 offset:2048
	ds_read_b128 v[166:169], v166 offset:3072
	s_mov_b32 m0, s59
	v_lshl_add_u64 v[206:207], v[204:205], 0, s[60:61]
	ds_read_b128 v[170:173], v135 offset:32768
	ds_read_b128 v[174:177], v135 offset:33792
	ds_read_b128 v[178:181], v135 offset:34816
	ds_read_b128 v[182:185], v135 offset:35840
	ds_read_b128 v[186:189], v135 offset:36864
	ds_read_b128 v[190:193], v135 offset:37888
	ds_read_b128 v[194:197], v135 offset:38912
	ds_read_b128 v[198:201], v135 offset:39936
	global_load_lds_dwordx4 v[206:207], off
	v_lshl_add_u64 v[206:207], v[204:205], 0, s[52:53]
	s_mov_b32 m0, s63
	s_nop 0
	global_load_lds_dwordx4 v[206:207], off
	s_waitcnt vmcnt(8)
	s_waitcnt lgkmcnt(0)
	s_barrier
	s_setprio 1
	v_mfma_f32_16x16x32_bf16 v[124:127], v[136:139], v[170:173], v[124:127]
	v_mfma_f32_16x16x32_bf16 v[120:123], v[144:147], v[170:173], v[120:123]
	v_mfma_f32_16x16x32_bf16 v[108:111], v[136:139], v[178:181], v[108:111]
	v_mfma_f32_16x16x32_bf16 v[104:107], v[144:147], v[178:181], v[104:107]
	v_mfma_f32_16x16x32_bf16 v[92:95], v[136:139], v[186:189], v[92:95]
	v_mfma_f32_16x16x32_bf16 v[88:91], v[144:147], v[186:189], v[88:91]
	v_mfma_f32_16x16x32_bf16 v[76:79], v[136:139], v[194:197], v[76:79]
	v_mfma_f32_16x16x32_bf16 v[72:75], v[144:147], v[194:197], v[72:75]
	v_mfma_f32_16x16x32_bf16 v[124:127], v[140:143], v[174:177], v[124:127]
	v_mfma_f32_16x16x32_bf16 v[120:123], v[148:151], v[174:177], v[120:123]
	v_mfma_f32_16x16x32_bf16 v[108:111], v[140:143], v[182:185], v[108:111]
	v_mfma_f32_16x16x32_bf16 v[104:107], v[148:151], v[182:185], v[104:107]
	v_mfma_f32_16x16x32_bf16 v[92:95], v[140:143], v[190:193], v[92:95]
	v_mfma_f32_16x16x32_bf16 v[88:91], v[148:151], v[190:193], v[88:91]
	v_mfma_f32_16x16x32_bf16 v[76:79], v[140:143], v[198:201], v[76:79]
	v_mfma_f32_16x16x32_bf16 v[72:75], v[148:151], v[198:201], v[72:75]
	v_mfma_f32_16x16x32_bf16 v[116:119], v[152:155], v[170:173], v[116:119]
	v_mfma_f32_16x16x32_bf16 v[112:115], v[162:165], v[170:173], v[112:115]
	v_mfma_f32_16x16x32_bf16 v[100:103], v[152:155], v[178:181], v[100:103]
	v_mfma_f32_16x16x32_bf16 v[96:99], v[162:165], v[178:181], v[96:99]
	v_mfma_f32_16x16x32_bf16 v[84:87], v[152:155], v[186:189], v[84:87]
	v_mfma_f32_16x16x32_bf16 v[80:83], v[162:165], v[186:189], v[80:83]
	v_mfma_f32_16x16x32_bf16 v[68:71], v[152:155], v[194:197], v[68:71]
	v_mfma_f32_16x16x32_bf16 v[64:67], v[162:165], v[194:197], v[64:67]
	v_mfma_f32_16x16x32_bf16 v[116:119], v[156:159], v[174:177], v[116:119]
	v_mfma_f32_16x16x32_bf16 v[112:115], v[166:169], v[174:177], v[112:115]
	v_mfma_f32_16x16x32_bf16 v[100:103], v[156:159], v[182:185], v[100:103]
	v_mfma_f32_16x16x32_bf16 v[96:99], v[166:169], v[182:185], v[96:99]
	v_mfma_f32_16x16x32_bf16 v[84:87], v[156:159], v[190:193], v[84:87]
	v_mfma_f32_16x16x32_bf16 v[80:83], v[166:169], v[190:193], v[80:83]
	v_mfma_f32_16x16x32_bf16 v[68:71], v[156:159], v[198:201], v[68:71]
	v_mfma_f32_16x16x32_bf16 v[64:67], v[166:169], v[198:201], v[64:67]
	s_setprio 0
	s_barrier
	s_add_i32 s2, s2, s31
	v_lshl_add_u64 v[206:207], v[202:203], 0, s[56:57]
	s_mov_b32 m0, s2
	ds_read_b128 v[170:173], v135 offset:49152
	ds_read_b128 v[174:177], v135 offset:50176
	ds_read_b128 v[178:181], v135 offset:51200
	ds_read_b128 v[182:185], v135 offset:52224
	ds_read_b128 v[186:189], v135 offset:53248
	ds_read_b128 v[190:193], v135 offset:54272
	ds_read_b128 v[194:197], v135 offset:55296
	ds_read_b128 v[198:201], v135 offset:56320
	global_load_lds_dwordx4 v[206:207], off
	v_lshl_add_u64 v[206:207], v[202:203], 0, s[0:1]
	s_add_i32 m0, s2, 0x2000
	s_add_i32 s2, s3, s31
	global_load_lds_dwordx4 v[206:207], off
	v_lshl_add_u64 v[206:207], v[202:203], 0, s[24:25]
	s_mov_b32 m0, s2
	v_lshl_add_u64 v[202:203], v[202:203], 0, s[26:27]
	global_load_lds_dwordx4 v[206:207], off
	s_add_i32 m0, s2, 0x2000
	s_nop 0
	global_load_lds_dwordx4 v[202:203], off
	v_lshl_add_u64 v[202:203], v[204:205], 0, s[56:57]
	s_mov_b32 m0, s77
	s_nop 0
	global_load_lds_dwordx4 v[202:203], off
	v_lshl_add_u64 v[202:203], v[204:205], 0, s[0:1]
	s_mov_b32 m0, s78
	s_nop 0
	global_load_lds_dwordx4 v[202:203], off
	s_waitcnt vmcnt(8)
	s_waitcnt lgkmcnt(0)
	s_barrier
	s_setprio 1
	v_mfma_f32_16x16x32_bf16 v[60:63], v[136:139], v[170:173], v[60:63]
	v_mfma_f32_16x16x32_bf16 v[56:59], v[144:147], v[170:173], v[56:59]
	v_mfma_f32_16x16x32_bf16 v[44:47], v[136:139], v[178:181], v[44:47]
	v_mfma_f32_16x16x32_bf16 v[40:43], v[144:147], v[178:181], v[40:43]
	v_mfma_f32_16x16x32_bf16 v[28:31], v[136:139], v[186:189], v[28:31]
	v_mfma_f32_16x16x32_bf16 v[24:27], v[144:147], v[186:189], v[24:27]
	v_mfma_f32_16x16x32_bf16 v[12:15], v[136:139], v[194:197], v[12:15]
	v_mfma_f32_16x16x32_bf16 v[8:11], v[144:147], v[194:197], v[8:11]
	v_mfma_f32_16x16x32_bf16 v[60:63], v[140:143], v[174:177], v[60:63]
	v_mfma_f32_16x16x32_bf16 v[56:59], v[148:151], v[174:177], v[56:59]
	v_mfma_f32_16x16x32_bf16 v[44:47], v[140:143], v[182:185], v[44:47]
	v_mfma_f32_16x16x32_bf16 v[40:43], v[148:151], v[182:185], v[40:43]
	v_mfma_f32_16x16x32_bf16 v[28:31], v[140:143], v[190:193], v[28:31]
	v_mfma_f32_16x16x32_bf16 v[24:27], v[148:151], v[190:193], v[24:27]
	v_mfma_f32_16x16x32_bf16 v[12:15], v[140:143], v[198:201], v[12:15]
	v_mfma_f32_16x16x32_bf16 v[8:11], v[148:151], v[198:201], v[8:11]
	v_mfma_f32_16x16x32_bf16 v[52:55], v[152:155], v[170:173], v[52:55]
	v_mfma_f32_16x16x32_bf16 v[48:51], v[162:165], v[170:173], v[48:51]
	v_mfma_f32_16x16x32_bf16 v[36:39], v[152:155], v[178:181], v[36:39]
	v_mfma_f32_16x16x32_bf16 v[32:35], v[162:165], v[178:181], v[32:35]
	v_mfma_f32_16x16x32_bf16 v[20:23], v[152:155], v[186:189], v[20:23]
	v_mfma_f32_16x16x32_bf16 v[16:19], v[162:165], v[186:189], v[16:19]
	v_mfma_f32_16x16x32_bf16 v[4:7], v[152:155], v[194:197], v[4:7]
	v_mfma_f32_16x16x32_bf16 v[0:3], v[162:165], v[194:197], v[0:3]
	v_mfma_f32_16x16x32_bf16 v[52:55], v[156:159], v[174:177], v[52:55]
	v_mfma_f32_16x16x32_bf16 v[48:51], v[166:169], v[174:177], v[48:51]
	v_mfma_f32_16x16x32_bf16 v[36:39], v[156:159], v[182:185], v[36:39]
	v_mfma_f32_16x16x32_bf16 v[32:35], v[166:169], v[182:185], v[32:35]
	v_mfma_f32_16x16x32_bf16 v[20:23], v[156:159], v[190:193], v[20:23]
	v_mfma_f32_16x16x32_bf16 v[16:19], v[166:169], v[190:193], v[16:19]
	v_mfma_f32_16x16x32_bf16 v[4:7], v[156:159], v[198:201], v[4:7]
	v_mfma_f32_16x16x32_bf16 v[0:3], v[166:169], v[198:201], v[0:3]
	s_setprio 0
	s_barrier
	s_add_u32 s74, s74, 0x100
	s_addc_u32 s75, s75, 0
	s_add_u32 s22, s22, 0x100
	s_addc_u32 s23, s23, 0
	s_cmp_ge_i32 s38, s79
	s_mov_b32 s2, s38
	s_cbranch_scc0 .LBB0_189

.LBB0_206:
	s_add_i32 s38, s2, 2
	s_add_u32 s39, s54, 0xfffc0080
	s_addc_u32 s3, s55, -1
	s_cmp_eq_u32 s78, s2
	s_cselect_b32 s3, s43, s3
	s_cselect_b32 s2, s45, s39
	s_cselect_b32 s87, s81, s23
	s_cselect_b32 s86, s83, s22
	s_add_i32 s39, 0, 0x10000
	s_add_i32 s90, 0, 0x14000
	v_add_u32_e32 v148, s39, v133
	v_add_u32_e32 v166, s90, v133
	ds_read_b128 v[136:139], v148
	ds_read_b128 v[140:143], v148 offset:1024
	ds_read_b128 v[144:147], v148 offset:2048
	ds_read_b128 v[148:151], v148 offset:3072
	ds_read_b128 v[152:155], v166
	ds_read_b128 v[156:159], v166 offset:1024
	ds_read_b128 v[162:165], v166 offset:2048
	ds_read_b128 v[166:169], v166 offset:3072
	v_lshl_add_u64 v[202:203], s[54:55], 0, v[130:131]
	s_add_i32 m0, s33, 0xc000
	ds_read_b128 v[170:173], v135
	ds_read_b128 v[174:177], v135 offset:1024
	ds_read_b128 v[178:181], v135 offset:2048
	ds_read_b128 v[182:185], v135 offset:3072
	ds_read_b128 v[186:189], v135 offset:4096
	ds_read_b128 v[190:193], v135 offset:5120
	ds_read_b128 v[194:197], v135 offset:6144
	ds_read_b128 v[198:201], v135 offset:7168
	global_load_lds_dwordx4 v[202:203], off
	v_lshl_add_u64 v[202:203], v[202:203], 0, s[14:15]
	s_add_i32 m0, s33, 0xe000
	s_nop 0
	global_load_lds_dwordx4 v[202:203], off
	s_waitcnt vmcnt(8)
	s_waitcnt lgkmcnt(0)
	s_barrier
	s_setprio 1
	v_mfma_f32_16x16x32_bf16 v[124:127], v[136:139], v[170:173], v[124:127]
	v_mfma_f32_16x16x32_bf16 v[120:123], v[144:147], v[170:173], v[120:123]
	v_mfma_f32_16x16x32_bf16 v[108:111], v[136:139], v[178:181], v[108:111]
	v_mfma_f32_16x16x32_bf16 v[104:107], v[144:147], v[178:181], v[104:107]
	v_mfma_f32_16x16x32_bf16 v[92:95], v[136:139], v[186:189], v[92:95]
	v_mfma_f32_16x16x32_bf16 v[88:91], v[144:147], v[186:189], v[88:91]
	v_mfma_f32_16x16x32_bf16 v[76:79], v[136:139], v[194:197], v[76:79]
	v_mfma_f32_16x16x32_bf16 v[72:75], v[144:147], v[194:197], v[72:75]
	v_mfma_f32_16x16x32_bf16 v[124:127], v[140:143], v[174:177], v[124:127]
	v_mfma_f32_16x16x32_bf16 v[120:123], v[148:151], v[174:177], v[120:123]
	v_mfma_f32_16x16x32_bf16 v[108:111], v[140:143], v[182:185], v[108:111]
	v_mfma_f32_16x16x32_bf16 v[104:107], v[148:151], v[182:185], v[104:107]
	v_mfma_f32_16x16x32_bf16 v[92:95], v[140:143], v[190:193], v[92:95]
	v_mfma_f32_16x16x32_bf16 v[88:91], v[148:151], v[190:193], v[88:91]
	v_mfma_f32_16x16x32_bf16 v[76:79], v[140:143], v[198:201], v[76:79]
	v_mfma_f32_16x16x32_bf16 v[72:75], v[148:151], v[198:201], v[72:75]
	v_mfma_f32_16x16x32_bf16 v[116:119], v[152:155], v[170:173], v[116:119]
	v_mfma_f32_16x16x32_bf16 v[112:115], v[162:165], v[170:173], v[112:115]
	v_mfma_f32_16x16x32_bf16 v[100:103], v[152:155], v[178:181], v[100:103]
	v_mfma_f32_16x16x32_bf16 v[96:99], v[162:165], v[178:181], v[96:99]
	v_mfma_f32_16x16x32_bf16 v[84:87], v[152:155], v[186:189], v[84:87]
	v_mfma_f32_16x16x32_bf16 v[80:83], v[162:165], v[186:189], v[80:83]
	v_mfma_f32_16x16x32_bf16 v[68:71], v[152:155], v[194:197], v[68:71]
	v_mfma_f32_16x16x32_bf16 v[64:67], v[162:165], v[194:197], v[64:67]
	v_mfma_f32_16x16x32_bf16 v[116:119], v[156:159], v[174:177], v[116:119]
	v_mfma_f32_16x16x32_bf16 v[112:115], v[166:169], v[174:177], v[112:115]
	v_mfma_f32_16x16x32_bf16 v[100:103], v[156:159], v[182:185], v[100:103]
	v_mfma_f32_16x16x32_bf16 v[96:99], v[166:169], v[182:185], v[96:99]
	v_mfma_f32_16x16x32_bf16 v[84:87], v[156:159], v[190:193], v[84:87]
	v_mfma_f32_16x16x32_bf16 v[80:83], v[166:169], v[190:193], v[80:83]
	v_mfma_f32_16x16x32_bf16 v[68:71], v[156:159], v[198:201], v[68:71]
	v_mfma_f32_16x16x32_bf16 v[64:67], v[166:169], v[198:201], v[64:67]
	s_setprio 0
	s_barrier
	s_add_i32 s39, s39, s10
	v_lshl_add_u64 v[202:203], s[86:87], 0, v[160:161]
	s_mov_b32 m0, s39
	ds_read_b128 v[170:173], v135 offset:16384
	ds_read_b128 v[174:177], v135 offset:17408
	ds_read_b128 v[178:181], v135 offset:18432
	ds_read_b128 v[182:185], v135 offset:19456
	ds_read_b128 v[186:189], v135 offset:20480
	ds_read_b128 v[190:193], v135 offset:21504
	ds_read_b128 v[194:197], v135 offset:22528
	ds_read_b128 v[198:201], v135 offset:23552
	global_load_lds_dwordx4 v[202:203], off
	v_lshl_add_u64 v[204:205], v[202:203], 0, s[14:15]
	s_add_i32 m0, s39, 0x2000
	s_add_i32 s39, s90, s10
	global_load_lds_dwordx4 v[204:205], off
	v_lshl_add_u64 v[204:205], v[202:203], 0, s[60:61]
	s_mov_b32 m0, s39
	s_nop 0
	global_load_lds_dwordx4 v[204:205], off
	v_lshl_add_u64 v[204:205], v[202:203], 0, s[52:53]
	s_add_i32 m0, s39, 0x2000
	s_nop 0
	global_load_lds_dwordx4 v[204:205], off
	v_lshl_add_u64 v[204:205], s[2:3], 0, v[128:129]
	s_mov_b32 m0, s33
	v_lshl_add_u64 v[206:207], v[204:205], 0, s[14:15]
	global_load_lds_dwordx4 v[204:205], off
	s_mov_b32 m0, s58
	s_nop 0
	global_load_lds_dwordx4 v[206:207], off
	s_waitcnt vmcnt(8)
	s_waitcnt lgkmcnt(0)
	s_barrier
	s_setprio 1
	v_mfma_f32_16x16x32_bf16 v[60:63], v[136:139], v[170:173], v[60:63]
	v_mfma_f32_16x16x32_bf16 v[56:59], v[144:147], v[170:173], v[56:59]
	v_mfma_f32_16x16x32_bf16 v[44:47], v[136:139], v[178:181], v[44:47]
	v_mfma_f32_16x16x32_bf16 v[40:43], v[144:147], v[178:181], v[40:43]
	v_mfma_f32_16x16x32_bf16 v[28:31], v[136:139], v[186:189], v[28:31]
	v_mfma_f32_16x16x32_bf16 v[24:27], v[144:147], v[186:189], v[24:27]
	v_mfma_f32_16x16x32_bf16 v[12:15], v[136:139], v[194:197], v[12:15]
	v_mfma_f32_16x16x32_bf16 v[8:11], v[144:147], v[194:197], v[8:11]
	v_mfma_f32_16x16x32_bf16 v[60:63], v[140:143], v[174:177], v[60:63]
	v_mfma_f32_16x16x32_bf16 v[56:59], v[148:151], v[174:177], v[56:59]
	v_mfma_f32_16x16x32_bf16 v[44:47], v[140:143], v[182:185], v[44:47]
	v_mfma_f32_16x16x32_bf16 v[40:43], v[148:151], v[182:185], v[40:43]
	v_mfma_f32_16x16x32_bf16 v[28:31], v[140:143], v[190:193], v[28:31]
	v_mfma_f32_16x16x32_bf16 v[24:27], v[148:151], v[190:193], v[24:27]
	v_mfma_f32_16x16x32_bf16 v[12:15], v[140:143], v[198:201], v[12:15]
	v_mfma_f32_16x16x32_bf16 v[8:11], v[148:151], v[198:201], v[8:11]
	v_mfma_f32_16x16x32_bf16 v[52:55], v[152:155], v[170:173], v[52:55]
	v_mfma_f32_16x16x32_bf16 v[48:51], v[162:165], v[170:173], v[48:51]
	v_mfma_f32_16x16x32_bf16 v[36:39], v[152:155], v[178:181], v[36:39]
	v_mfma_f32_16x16x32_bf16 v[32:35], v[162:165], v[178:181], v[32:35]
	v_mfma_f32_16x16x32_bf16 v[20:23], v[152:155], v[186:189], v[20:23]
	v_mfma_f32_16x16x32_bf16 v[16:19], v[162:165], v[186:189], v[16:19]
	v_mfma_f32_16x16x32_bf16 v[4:7], v[152:155], v[194:197], v[4:7]
	v_mfma_f32_16x16x32_bf16 v[0:3], v[162:165], v[194:197], v[0:3]
	v_mfma_f32_16x16x32_bf16 v[52:55], v[156:159], v[174:177], v[52:55]
	v_mfma_f32_16x16x32_bf16 v[48:51], v[166:169], v[174:177], v[48:51]
	v_mfma_f32_16x16x32_bf16 v[36:39], v[156:159], v[182:185], v[36:39]
	v_mfma_f32_16x16x32_bf16 v[32:35], v[166:169], v[182:185], v[32:35]
	v_mfma_f32_16x16x32_bf16 v[20:23], v[156:159], v[190:193], v[20:23]
	v_mfma_f32_16x16x32_bf16 v[16:19], v[166:169], v[190:193], v[16:19]
	v_mfma_f32_16x16x32_bf16 v[4:7], v[156:159], v[198:201], v[4:7]
	v_mfma_f32_16x16x32_bf16 v[0:3], v[166:169], v[198:201], v[0:3]
	s_setprio 0
	s_barrier
	s_add_i32 s2, 0, 0x18000
	s_add_i32 s3, 0, 0x1c000
	v_add_u32_e32 v148, s2, v133
	v_add_u32_e32 v166, s3, v133
	ds_read_b128 v[136:139], v148
	ds_read_b128 v[140:143], v148 offset:1024
	ds_read_b128 v[144:147], v148 offset:2048
	ds_read_b128 v[148:151], v148 offset:3072
	ds_read_b128 v[152:155], v166
	ds_read_b128 v[156:159], v166 offset:1024
	ds_read_b128 v[162:165], v166 offset:2048
	ds_read_b128 v[166:169], v166 offset:3072
	s_mov_b32 m0, s59
	v_lshl_add_u64 v[206:207], v[204:205], 0, s[60:61]
	ds_read_b128 v[170:173], v135 offset:32768
	ds_read_b128 v[174:177], v135 offset:33792
	ds_read_b128 v[178:181], v135 offset:34816
	ds_read_b128 v[182:185], v135 offset:35840
	ds_read_b128 v[186:189], v135 offset:36864
	ds_read_b128 v[190:193], v135 offset:37888
	ds_read_b128 v[194:197], v135 offset:38912
	ds_read_b128 v[198:201], v135 offset:39936
	global_load_lds_dwordx4 v[206:207], off
	v_lshl_add_u64 v[206:207], v[204:205], 0, s[52:53]
	s_mov_b32 m0, s63
	s_nop 0
	global_load_lds_dwordx4 v[206:207], off
	s_waitcnt vmcnt(8)
	s_waitcnt lgkmcnt(0)
	s_barrier
	s_setprio 1
	v_mfma_f32_16x16x32_bf16 v[124:127], v[136:139], v[170:173], v[124:127]
	v_mfma_f32_16x16x32_bf16 v[120:123], v[144:147], v[170:173], v[120:123]
	v_mfma_f32_16x16x32_bf16 v[108:111], v[136:139], v[178:181], v[108:111]
	v_mfma_f32_16x16x32_bf16 v[104:107], v[144:147], v[178:181], v[104:107]
	v_mfma_f32_16x16x32_bf16 v[92:95], v[136:139], v[186:189], v[92:95]
	v_mfma_f32_16x16x32_bf16 v[88:91], v[144:147], v[186:189], v[88:91]
	v_mfma_f32_16x16x32_bf16 v[76:79], v[136:139], v[194:197], v[76:79]
	v_mfma_f32_16x16x32_bf16 v[72:75], v[144:147], v[194:197], v[72:75]
	v_mfma_f32_16x16x32_bf16 v[124:127], v[140:143], v[174:177], v[124:127]
	v_mfma_f32_16x16x32_bf16 v[120:123], v[148:151], v[174:177], v[120:123]
	v_mfma_f32_16x16x32_bf16 v[108:111], v[140:143], v[182:185], v[108:111]
	v_mfma_f32_16x16x32_bf16 v[104:107], v[148:151], v[182:185], v[104:107]
	v_mfma_f32_16x16x32_bf16 v[92:95], v[140:143], v[190:193], v[92:95]
	v_mfma_f32_16x16x32_bf16 v[88:91], v[148:151], v[190:193], v[88:91]
	v_mfma_f32_16x16x32_bf16 v[76:79], v[140:143], v[198:201], v[76:79]
	v_mfma_f32_16x16x32_bf16 v[72:75], v[148:151], v[198:201], v[72:75]
	v_mfma_f32_16x16x32_bf16 v[116:119], v[152:155], v[170:173], v[116:119]
	v_mfma_f32_16x16x32_bf16 v[112:115], v[162:165], v[170:173], v[112:115]
	v_mfma_f32_16x16x32_bf16 v[100:103], v[152:155], v[178:181], v[100:103]
	v_mfma_f32_16x16x32_bf16 v[96:99], v[162:165], v[178:181], v[96:99]
	v_mfma_f32_16x16x32_bf16 v[84:87], v[152:155], v[186:189], v[84:87]
	v_mfma_f32_16x16x32_bf16 v[80:83], v[162:165], v[186:189], v[80:83]
	v_mfma_f32_16x16x32_bf16 v[68:71], v[152:155], v[194:197], v[68:71]
	v_mfma_f32_16x16x32_bf16 v[64:67], v[162:165], v[194:197], v[64:67]
	v_mfma_f32_16x16x32_bf16 v[116:119], v[156:159], v[174:177], v[116:119]
	v_mfma_f32_16x16x32_bf16 v[112:115], v[166:169], v[174:177], v[112:115]
	v_mfma_f32_16x16x32_bf16 v[100:103], v[156:159], v[182:185], v[100:103]
	v_mfma_f32_16x16x32_bf16 v[96:99], v[166:169], v[182:185], v[96:99]
	v_mfma_f32_16x16x32_bf16 v[84:87], v[156:159], v[190:193], v[84:87]
	v_mfma_f32_16x16x32_bf16 v[80:83], v[166:169], v[190:193], v[80:83]
	v_mfma_f32_16x16x32_bf16 v[68:71], v[156:159], v[198:201], v[68:71]
	v_mfma_f32_16x16x32_bf16 v[64:67], v[166:169], v[198:201], v[64:67]
	s_setprio 0
	s_barrier
	s_add_i32 s2, s2, s10
	v_lshl_add_u64 v[206:207], v[202:203], 0, s[56:57]
	s_mov_b32 m0, s2
	ds_read_b128 v[170:173], v135 offset:49152
	ds_read_b128 v[174:177], v135 offset:50176
	ds_read_b128 v[178:181], v135 offset:51200
	ds_read_b128 v[182:185], v135 offset:52224
	ds_read_b128 v[186:189], v135 offset:53248
	ds_read_b128 v[190:193], v135 offset:54272
	ds_read_b128 v[194:197], v135 offset:55296
	ds_read_b128 v[198:201], v135 offset:56320
	global_load_lds_dwordx4 v[206:207], off
	v_lshl_add_u64 v[206:207], v[202:203], 0, s[0:1]
	s_add_i32 m0, s2, 0x2000
	s_add_i32 s2, s3, s10
	global_load_lds_dwordx4 v[206:207], off
	v_lshl_add_u64 v[206:207], v[202:203], 0, s[24:25]
	s_mov_b32 m0, s2
	v_lshl_add_u64 v[202:203], v[202:203], 0, s[26:27]
	global_load_lds_dwordx4 v[206:207], off
	s_add_i32 m0, s2, 0x2000
	s_nop 0
	global_load_lds_dwordx4 v[202:203], off
	v_lshl_add_u64 v[202:203], v[204:205], 0, s[56:57]
	s_mov_b32 m0, s75
	s_nop 0
	global_load_lds_dwordx4 v[202:203], off
	v_lshl_add_u64 v[202:203], v[204:205], 0, s[0:1]
	s_mov_b32 m0, s77
	s_nop 0
	global_load_lds_dwordx4 v[202:203], off
	s_waitcnt vmcnt(8)
	s_waitcnt lgkmcnt(0)
	s_barrier
	s_setprio 1
	v_mfma_f32_16x16x32_bf16 v[60:63], v[136:139], v[170:173], v[60:63]
	v_mfma_f32_16x16x32_bf16 v[56:59], v[144:147], v[170:173], v[56:59]
	v_mfma_f32_16x16x32_bf16 v[44:47], v[136:139], v[178:181], v[44:47]
	v_mfma_f32_16x16x32_bf16 v[40:43], v[144:147], v[178:181], v[40:43]
	v_mfma_f32_16x16x32_bf16 v[28:31], v[136:139], v[186:189], v[28:31]
	v_mfma_f32_16x16x32_bf16 v[24:27], v[144:147], v[186:189], v[24:27]
	v_mfma_f32_16x16x32_bf16 v[12:15], v[136:139], v[194:197], v[12:15]
	v_mfma_f32_16x16x32_bf16 v[8:11], v[144:147], v[194:197], v[8:11]
	v_mfma_f32_16x16x32_bf16 v[60:63], v[140:143], v[174:177], v[60:63]
	v_mfma_f32_16x16x32_bf16 v[56:59], v[148:151], v[174:177], v[56:59]
	v_mfma_f32_16x16x32_bf16 v[44:47], v[140:143], v[182:185], v[44:47]
	v_mfma_f32_16x16x32_bf16 v[40:43], v[148:151], v[182:185], v[40:43]
	v_mfma_f32_16x16x32_bf16 v[28:31], v[140:143], v[190:193], v[28:31]
	v_mfma_f32_16x16x32_bf16 v[24:27], v[148:151], v[190:193], v[24:27]
	v_mfma_f32_16x16x32_bf16 v[12:15], v[140:143], v[198:201], v[12:15]
	v_mfma_f32_16x16x32_bf16 v[8:11], v[148:151], v[198:201], v[8:11]
	v_mfma_f32_16x16x32_bf16 v[52:55], v[152:155], v[170:173], v[52:55]
	v_mfma_f32_16x16x32_bf16 v[48:51], v[162:165], v[170:173], v[48:51]
	v_mfma_f32_16x16x32_bf16 v[36:39], v[152:155], v[178:181], v[36:39]
	v_mfma_f32_16x16x32_bf16 v[32:35], v[162:165], v[178:181], v[32:35]
	v_mfma_f32_16x16x32_bf16 v[20:23], v[152:155], v[186:189], v[20:23]
	v_mfma_f32_16x16x32_bf16 v[16:19], v[162:165], v[186:189], v[16:19]
	v_mfma_f32_16x16x32_bf16 v[4:7], v[152:155], v[194:197], v[4:7]
	v_mfma_f32_16x16x32_bf16 v[0:3], v[162:165], v[194:197], v[0:3]
	v_mfma_f32_16x16x32_bf16 v[52:55], v[156:159], v[174:177], v[52:55]
	v_mfma_f32_16x16x32_bf16 v[48:51], v[166:169], v[174:177], v[48:51]
	v_mfma_f32_16x16x32_bf16 v[36:39], v[156:159], v[182:185], v[36:39]
	v_mfma_f32_16x16x32_bf16 v[32:35], v[166:169], v[182:185], v[32:35]
	v_mfma_f32_16x16x32_bf16 v[20:23], v[156:159], v[190:193], v[20:23]
	v_mfma_f32_16x16x32_bf16 v[16:19], v[166:169], v[190:193], v[16:19]
	v_mfma_f32_16x16x32_bf16 v[4:7], v[156:159], v[198:201], v[4:7]
	v_mfma_f32_16x16x32_bf16 v[0:3], v[166:169], v[198:201], v[0:3]
	s_setprio 0
	s_barrier
	s_add_u32 s54, s54, 0x100
	s_addc_u32 s55, s55, 0
	s_add_u32 s22, s22, 0x100
	s_addc_u32 s23, s23, 0
	s_cmp_ge_i32 s38, s74
	s_mov_b32 s2, s38
	s_cbranch_scc0 .LBB0_206

.LBB0_339:
	s_add_i32 s22, s2, 2
	s_add_u32 s23, s90, 0xfffe0080
	s_addc_u32 s3, s91, -1
	s_cmp_eq_u32 s83, s2
	s_cselect_b32 s3, s47, s3
	s_cselect_b32 s2, s93, s23
	s_cselect_b32 s35, s95, s38
	s_cselect_b32 s34, vcc_lo, vcc_hi
	s_add_i32 s23, 0, 0x10000
	s_add_i32 s39, 0, 0x14000
	v_add_u32_e32 v148, s23, v133
	v_add_u32_e32 v166, s39, v133
	ds_read_b128 v[136:139], v148
	ds_read_b128 v[140:143], v148 offset:1024
	ds_read_b128 v[144:147], v148 offset:2048
	ds_read_b128 v[148:151], v148 offset:3072
	ds_read_b128 v[152:155], v166
	ds_read_b128 v[156:159], v166 offset:1024
	ds_read_b128 v[162:165], v166 offset:2048
	ds_read_b128 v[166:169], v166 offset:3072
	v_lshl_add_u64 v[202:203], s[90:91], 0, v[130:131]
	s_add_i32 m0, s59, 0xc000
	ds_read_b128 v[170:173], v135
	ds_read_b128 v[174:177], v135 offset:1024
	ds_read_b128 v[178:181], v135 offset:2048
	ds_read_b128 v[182:185], v135 offset:3072
	ds_read_b128 v[186:189], v135 offset:4096
	ds_read_b128 v[190:193], v135 offset:5120
	ds_read_b128 v[194:197], v135 offset:6144
	ds_read_b128 v[198:201], v135 offset:7168
	global_load_lds_dwordx4 v[202:203], off
	v_lshl_add_u64 v[202:203], v[202:203], 0, s[8:9]
	s_add_i32 m0, s59, 0xe000
	s_nop 0
	global_load_lds_dwordx4 v[202:203], off
	s_waitcnt vmcnt(8)
	s_waitcnt lgkmcnt(0)
	s_barrier
	s_setprio 1
	v_mfma_f32_16x16x32_bf16 v[124:127], v[136:139], v[170:173], v[124:127]
	v_mfma_f32_16x16x32_bf16 v[120:123], v[144:147], v[170:173], v[120:123]
	v_mfma_f32_16x16x32_bf16 v[108:111], v[136:139], v[178:181], v[108:111]
	v_mfma_f32_16x16x32_bf16 v[104:107], v[144:147], v[178:181], v[104:107]
	v_mfma_f32_16x16x32_bf16 v[92:95], v[136:139], v[186:189], v[92:95]
	v_mfma_f32_16x16x32_bf16 v[88:91], v[144:147], v[186:189], v[88:91]
	v_mfma_f32_16x16x32_bf16 v[76:79], v[136:139], v[194:197], v[76:79]
	v_mfma_f32_16x16x32_bf16 v[72:75], v[144:147], v[194:197], v[72:75]
	v_mfma_f32_16x16x32_bf16 v[124:127], v[140:143], v[174:177], v[124:127]
	v_mfma_f32_16x16x32_bf16 v[120:123], v[148:151], v[174:177], v[120:123]
	v_mfma_f32_16x16x32_bf16 v[108:111], v[140:143], v[182:185], v[108:111]
	v_mfma_f32_16x16x32_bf16 v[104:107], v[148:151], v[182:185], v[104:107]
	v_mfma_f32_16x16x32_bf16 v[92:95], v[140:143], v[190:193], v[92:95]
	v_mfma_f32_16x16x32_bf16 v[88:91], v[148:151], v[190:193], v[88:91]
	v_mfma_f32_16x16x32_bf16 v[76:79], v[140:143], v[198:201], v[76:79]
	v_mfma_f32_16x16x32_bf16 v[72:75], v[148:151], v[198:201], v[72:75]
	v_mfma_f32_16x16x32_bf16 v[116:119], v[152:155], v[170:173], v[116:119]
	v_mfma_f32_16x16x32_bf16 v[112:115], v[162:165], v[170:173], v[112:115]
	v_mfma_f32_16x16x32_bf16 v[100:103], v[152:155], v[178:181], v[100:103]
	v_mfma_f32_16x16x32_bf16 v[96:99], v[162:165], v[178:181], v[96:99]
	v_mfma_f32_16x16x32_bf16 v[84:87], v[152:155], v[186:189], v[84:87]
	v_mfma_f32_16x16x32_bf16 v[80:83], v[162:165], v[186:189], v[80:83]
	v_mfma_f32_16x16x32_bf16 v[68:71], v[152:155], v[194:197], v[68:71]
	v_mfma_f32_16x16x32_bf16 v[64:67], v[162:165], v[194:197], v[64:67]
	v_mfma_f32_16x16x32_bf16 v[116:119], v[156:159], v[174:177], v[116:119]
	v_mfma_f32_16x16x32_bf16 v[112:115], v[166:169], v[174:177], v[112:115]
	v_mfma_f32_16x16x32_bf16 v[100:103], v[156:159], v[182:185], v[100:103]
	v_mfma_f32_16x16x32_bf16 v[96:99], v[166:169], v[182:185], v[96:99]
	v_mfma_f32_16x16x32_bf16 v[84:87], v[156:159], v[190:193], v[84:87]
	v_mfma_f32_16x16x32_bf16 v[80:83], v[166:169], v[190:193], v[80:83]
	v_mfma_f32_16x16x32_bf16 v[68:71], v[156:159], v[198:201], v[68:71]
	v_mfma_f32_16x16x32_bf16 v[64:67], v[166:169], v[198:201], v[64:67]
	s_setprio 0
	s_barrier
	s_add_i32 s23, s23, s58
	v_lshl_add_u64 v[202:203], s[34:35], 0, v[160:161]
	s_mov_b32 m0, s23
	ds_read_b128 v[170:173], v135 offset:16384
	ds_read_b128 v[174:177], v135 offset:17408
	ds_read_b128 v[178:181], v135 offset:18432
	ds_read_b128 v[182:185], v135 offset:19456
	ds_read_b128 v[186:189], v135 offset:20480
	ds_read_b128 v[190:193], v135 offset:21504
	ds_read_b128 v[194:197], v135 offset:22528
	ds_read_b128 v[198:201], v135 offset:23552
	global_load_lds_dwordx4 v[202:203], off
	v_lshl_add_u64 v[204:205], v[202:203], 0, s[64:65]
	s_add_i32 m0, s23, 0x2000
	s_add_i32 s23, s39, s58
	global_load_lds_dwordx4 v[204:205], off
	v_lshl_add_u64 v[204:205], v[202:203], 0, s[8:9]
	s_mov_b32 m0, s23
	s_nop 0
	global_load_lds_dwordx4 v[204:205], off
	v_lshl_add_u64 v[204:205], v[202:203], 0, s[4:5]
	s_add_i32 m0, s23, 0x2000
	s_nop 0
	global_load_lds_dwordx4 v[204:205], off
	v_lshl_add_u64 v[204:205], s[2:3], 0, v[128:129]
	s_mov_b32 m0, s59
	v_lshl_add_u64 v[206:207], v[204:205], 0, s[8:9]
	global_load_lds_dwordx4 v[204:205], off
	s_mov_b32 m0, s63
	s_nop 0
	global_load_lds_dwordx4 v[206:207], off
	s_waitcnt vmcnt(8)
	s_waitcnt lgkmcnt(0)
	s_barrier
	s_setprio 1
	v_mfma_f32_16x16x32_bf16 v[60:63], v[136:139], v[170:173], v[60:63]
	v_mfma_f32_16x16x32_bf16 v[56:59], v[144:147], v[170:173], v[56:59]
	v_mfma_f32_16x16x32_bf16 v[44:47], v[136:139], v[178:181], v[44:47]
	v_mfma_f32_16x16x32_bf16 v[40:43], v[144:147], v[178:181], v[40:43]
	v_mfma_f32_16x16x32_bf16 v[28:31], v[136:139], v[186:189], v[28:31]
	v_mfma_f32_16x16x32_bf16 v[24:27], v[144:147], v[186:189], v[24:27]
	v_mfma_f32_16x16x32_bf16 v[12:15], v[136:139], v[194:197], v[12:15]
	v_mfma_f32_16x16x32_bf16 v[8:11], v[144:147], v[194:197], v[8:11]
	v_mfma_f32_16x16x32_bf16 v[60:63], v[140:143], v[174:177], v[60:63]
	v_mfma_f32_16x16x32_bf16 v[56:59], v[148:151], v[174:177], v[56:59]
	v_mfma_f32_16x16x32_bf16 v[44:47], v[140:143], v[182:185], v[44:47]
	v_mfma_f32_16x16x32_bf16 v[40:43], v[148:151], v[182:185], v[40:43]
	v_mfma_f32_16x16x32_bf16 v[28:31], v[140:143], v[190:193], v[28:31]
	v_mfma_f32_16x16x32_bf16 v[24:27], v[148:151], v[190:193], v[24:27]
	v_mfma_f32_16x16x32_bf16 v[12:15], v[140:143], v[198:201], v[12:15]
	v_mfma_f32_16x16x32_bf16 v[8:11], v[148:151], v[198:201], v[8:11]
	v_mfma_f32_16x16x32_bf16 v[52:55], v[152:155], v[170:173], v[52:55]
	v_mfma_f32_16x16x32_bf16 v[48:51], v[162:165], v[170:173], v[48:51]
	v_mfma_f32_16x16x32_bf16 v[36:39], v[152:155], v[178:181], v[36:39]
	v_mfma_f32_16x16x32_bf16 v[32:35], v[162:165], v[178:181], v[32:35]
	v_mfma_f32_16x16x32_bf16 v[20:23], v[152:155], v[186:189], v[20:23]
	v_mfma_f32_16x16x32_bf16 v[16:19], v[162:165], v[186:189], v[16:19]
	v_mfma_f32_16x16x32_bf16 v[4:7], v[152:155], v[194:197], v[4:7]
	v_mfma_f32_16x16x32_bf16 v[0:3], v[162:165], v[194:197], v[0:3]
	v_mfma_f32_16x16x32_bf16 v[52:55], v[156:159], v[174:177], v[52:55]
	v_mfma_f32_16x16x32_bf16 v[48:51], v[166:169], v[174:177], v[48:51]
	v_mfma_f32_16x16x32_bf16 v[36:39], v[156:159], v[182:185], v[36:39]
	v_mfma_f32_16x16x32_bf16 v[32:35], v[166:169], v[182:185], v[32:35]
	v_mfma_f32_16x16x32_bf16 v[20:23], v[156:159], v[190:193], v[20:23]
	v_mfma_f32_16x16x32_bf16 v[16:19], v[166:169], v[190:193], v[16:19]
	v_mfma_f32_16x16x32_bf16 v[4:7], v[156:159], v[198:201], v[4:7]
	v_mfma_f32_16x16x32_bf16 v[0:3], v[166:169], v[198:201], v[0:3]
	s_setprio 0
	s_barrier
	s_add_i32 s2, 0, 0x18000
	s_add_i32 s3, 0, 0x1c000
	v_add_u32_e32 v148, s2, v133
	v_add_u32_e32 v166, s3, v133
	ds_read_b128 v[136:139], v148
	ds_read_b128 v[140:143], v148 offset:1024
	ds_read_b128 v[144:147], v148 offset:2048
	ds_read_b128 v[148:151], v148 offset:3072
	ds_read_b128 v[152:155], v166
	ds_read_b128 v[156:159], v166 offset:1024
	ds_read_b128 v[162:165], v166 offset:2048
	ds_read_b128 v[166:169], v166 offset:3072
	s_mov_b32 m0, s77
	v_lshl_add_u64 v[206:207], v[204:205], 0, s[14:15]
	ds_read_b128 v[170:173], v135 offset:32768
	ds_read_b128 v[174:177], v135 offset:33792
	ds_read_b128 v[178:181], v135 offset:34816
	ds_read_b128 v[182:185], v135 offset:35840
	ds_read_b128 v[186:189], v135 offset:36864
	ds_read_b128 v[190:193], v135 offset:37888
	ds_read_b128 v[194:197], v135 offset:38912
	ds_read_b128 v[198:201], v135 offset:39936
	global_load_lds_dwordx4 v[206:207], off
	v_lshl_add_u64 v[206:207], v[204:205], 0, s[16:17]
	s_mov_b32 m0, s78
	s_nop 0
	global_load_lds_dwordx4 v[206:207], off
	s_waitcnt vmcnt(8)
	s_waitcnt lgkmcnt(0)
	s_barrier
	s_setprio 1
	v_mfma_f32_16x16x32_bf16 v[124:127], v[136:139], v[170:173], v[124:127]
	v_mfma_f32_16x16x32_bf16 v[120:123], v[144:147], v[170:173], v[120:123]
	v_mfma_f32_16x16x32_bf16 v[108:111], v[136:139], v[178:181], v[108:111]
	v_mfma_f32_16x16x32_bf16 v[104:107], v[144:147], v[178:181], v[104:107]
	v_mfma_f32_16x16x32_bf16 v[92:95], v[136:139], v[186:189], v[92:95]
	v_mfma_f32_16x16x32_bf16 v[88:91], v[144:147], v[186:189], v[88:91]
	v_mfma_f32_16x16x32_bf16 v[76:79], v[136:139], v[194:197], v[76:79]
	v_mfma_f32_16x16x32_bf16 v[72:75], v[144:147], v[194:197], v[72:75]
	v_mfma_f32_16x16x32_bf16 v[124:127], v[140:143], v[174:177], v[124:127]
	v_mfma_f32_16x16x32_bf16 v[120:123], v[148:151], v[174:177], v[120:123]
	v_mfma_f32_16x16x32_bf16 v[108:111], v[140:143], v[182:185], v[108:111]
	v_mfma_f32_16x16x32_bf16 v[104:107], v[148:151], v[182:185], v[104:107]
	v_mfma_f32_16x16x32_bf16 v[92:95], v[140:143], v[190:193], v[92:95]
	v_mfma_f32_16x16x32_bf16 v[88:91], v[148:151], v[190:193], v[88:91]
	v_mfma_f32_16x16x32_bf16 v[76:79], v[140:143], v[198:201], v[76:79]
	v_mfma_f32_16x16x32_bf16 v[72:75], v[148:151], v[198:201], v[72:75]
	v_mfma_f32_16x16x32_bf16 v[116:119], v[152:155], v[170:173], v[116:119]
	v_mfma_f32_16x16x32_bf16 v[112:115], v[162:165], v[170:173], v[112:115]
	v_mfma_f32_16x16x32_bf16 v[100:103], v[152:155], v[178:181], v[100:103]
	v_mfma_f32_16x16x32_bf16 v[96:99], v[162:165], v[178:181], v[96:99]
	v_mfma_f32_16x16x32_bf16 v[84:87], v[152:155], v[186:189], v[84:87]
	v_mfma_f32_16x16x32_bf16 v[80:83], v[162:165], v[186:189], v[80:83]
	v_mfma_f32_16x16x32_bf16 v[68:71], v[152:155], v[194:197], v[68:71]
	v_mfma_f32_16x16x32_bf16 v[64:67], v[162:165], v[194:197], v[64:67]
	v_mfma_f32_16x16x32_bf16 v[116:119], v[156:159], v[174:177], v[116:119]
	v_mfma_f32_16x16x32_bf16 v[112:115], v[166:169], v[174:177], v[112:115]
	v_mfma_f32_16x16x32_bf16 v[100:103], v[156:159], v[182:185], v[100:103]
	v_mfma_f32_16x16x32_bf16 v[96:99], v[166:169], v[182:185], v[96:99]
	v_mfma_f32_16x16x32_bf16 v[84:87], v[156:159], v[190:193], v[84:87]
	v_mfma_f32_16x16x32_bf16 v[80:83], v[166:169], v[190:193], v[80:83]
	v_mfma_f32_16x16x32_bf16 v[68:71], v[156:159], v[198:201], v[68:71]
	v_mfma_f32_16x16x32_bf16 v[64:67], v[166:169], v[198:201], v[64:67]
	s_setprio 0
	s_barrier
	s_add_i32 s2, s2, s58
	v_lshl_add_u64 v[206:207], v[202:203], 0, s[56:57]
	s_mov_b32 m0, s2
	ds_read_b128 v[170:173], v135 offset:49152
	ds_read_b128 v[174:177], v135 offset:50176
	ds_read_b128 v[178:181], v135 offset:51200
	ds_read_b128 v[182:185], v135 offset:52224
	ds_read_b128 v[186:189], v135 offset:53248
	ds_read_b128 v[190:193], v135 offset:54272
	ds_read_b128 v[194:197], v135 offset:55296
	ds_read_b128 v[198:201], v135 offset:56320
	global_load_lds_dwordx4 v[206:207], off
	v_lshl_add_u64 v[206:207], v[202:203], 0, s[12:13]
	s_add_i32 m0, s2, 0x2000
	s_add_i32 s2, s3, s58
	global_load_lds_dwordx4 v[206:207], off
	v_lshl_add_u64 v[206:207], v[202:203], 0, s[28:29]
	s_mov_b32 m0, s2
	v_lshl_add_u64 v[202:203], v[202:203], 0, s[88:89]
	global_load_lds_dwordx4 v[206:207], off
	s_add_i32 m0, s2, 0x2000
	s_nop 0
	global_load_lds_dwordx4 v[202:203], off
	v_lshl_add_u64 v[202:203], v[204:205], 0, s[56:57]
	s_mov_b32 m0, s79
	s_nop 0
	global_load_lds_dwordx4 v[202:203], off
	v_lshl_add_u64 v[202:203], v[204:205], 0, s[28:29]
	s_mov_b32 m0, s80
	s_nop 0
	global_load_lds_dwordx4 v[202:203], off
	s_waitcnt vmcnt(8)
	s_waitcnt lgkmcnt(0)
	s_barrier
	s_setprio 1
	v_mfma_f32_16x16x32_bf16 v[60:63], v[136:139], v[170:173], v[60:63]
	v_mfma_f32_16x16x32_bf16 v[56:59], v[144:147], v[170:173], v[56:59]
	v_mfma_f32_16x16x32_bf16 v[44:47], v[136:139], v[178:181], v[44:47]
	v_mfma_f32_16x16x32_bf16 v[40:43], v[144:147], v[178:181], v[40:43]
	v_mfma_f32_16x16x32_bf16 v[28:31], v[136:139], v[186:189], v[28:31]
	v_mfma_f32_16x16x32_bf16 v[24:27], v[144:147], v[186:189], v[24:27]
	v_mfma_f32_16x16x32_bf16 v[12:15], v[136:139], v[194:197], v[12:15]
	v_mfma_f32_16x16x32_bf16 v[8:11], v[144:147], v[194:197], v[8:11]
	v_mfma_f32_16x16x32_bf16 v[60:63], v[140:143], v[174:177], v[60:63]
	v_mfma_f32_16x16x32_bf16 v[56:59], v[148:151], v[174:177], v[56:59]
	v_mfma_f32_16x16x32_bf16 v[44:47], v[140:143], v[182:185], v[44:47]
	v_mfma_f32_16x16x32_bf16 v[40:43], v[148:151], v[182:185], v[40:43]
	v_mfma_f32_16x16x32_bf16 v[28:31], v[140:143], v[190:193], v[28:31]
	v_mfma_f32_16x16x32_bf16 v[24:27], v[148:151], v[190:193], v[24:27]
	v_mfma_f32_16x16x32_bf16 v[12:15], v[140:143], v[198:201], v[12:15]
	v_mfma_f32_16x16x32_bf16 v[8:11], v[148:151], v[198:201], v[8:11]
	v_mfma_f32_16x16x32_bf16 v[52:55], v[152:155], v[170:173], v[52:55]
	v_mfma_f32_16x16x32_bf16 v[48:51], v[162:165], v[170:173], v[48:51]
	v_mfma_f32_16x16x32_bf16 v[36:39], v[152:155], v[178:181], v[36:39]
	v_mfma_f32_16x16x32_bf16 v[32:35], v[162:165], v[178:181], v[32:35]
	v_mfma_f32_16x16x32_bf16 v[20:23], v[152:155], v[186:189], v[20:23]
	v_mfma_f32_16x16x32_bf16 v[16:19], v[162:165], v[186:189], v[16:19]
	v_mfma_f32_16x16x32_bf16 v[4:7], v[152:155], v[194:197], v[4:7]
	v_mfma_f32_16x16x32_bf16 v[0:3], v[162:165], v[194:197], v[0:3]
	v_mfma_f32_16x16x32_bf16 v[52:55], v[156:159], v[174:177], v[52:55]
	v_mfma_f32_16x16x32_bf16 v[48:51], v[166:169], v[174:177], v[48:51]
	v_mfma_f32_16x16x32_bf16 v[36:39], v[156:159], v[182:185], v[36:39]
	v_mfma_f32_16x16x32_bf16 v[32:35], v[166:169], v[182:185], v[32:35]
	v_mfma_f32_16x16x32_bf16 v[20:23], v[156:159], v[190:193], v[20:23]
	v_mfma_f32_16x16x32_bf16 v[16:19], v[166:169], v[190:193], v[16:19]
	v_mfma_f32_16x16x32_bf16 v[4:7], v[156:159], v[198:201], v[4:7]
	v_mfma_f32_16x16x32_bf16 v[0:3], v[166:169], v[198:201], v[0:3]
	s_setprio 0
	s_barrier
	s_add_u32 vcc_hi, vcc_hi, 0x100
	s_addc_u32 s38, s38, 0
	s_add_u32 s90, s90, 0x100
	s_addc_u32 s91, s91, 0
	s_cmp_ge_i32 s22, s81
	s_mov_b32 s2, s22
	s_cbranch_scc0 .LBB0_339

.LBB0_865:
	s_add_i32 s45, s2, 2
	s_add_u32 s46, s22, 0xfff30080
	s_addc_u32 s3, s23, -1
	s_cmp_eq_u32 s80, s2
	s_cselect_b32 s3, s19, s3
	s_cselect_b32 s2, s18, s46
	s_cselect_b32 s47, s39, s44
	s_cselect_b32 s46, s42, s43
	s_add_i32 s55, 0, 0x10000
	s_add_i32 s90, 0, 0x14000
	v_add_u32_e32 v148, s55, v175
	v_add_u32_e32 v160, s90, v175
	ds_read_b128 v[136:139], v148
	ds_read_b128 v[140:143], v148 offset:1024
	ds_read_b128 v[144:147], v148 offset:2048
	ds_read_b128 v[148:151], v148 offset:3072
	ds_read_b128 v[152:155], v160
	ds_read_b128 v[156:159], v160 offset:1024
	ds_read_b128 v[162:165], v160 offset:2048
	ds_read_b128 v[166:169], v160 offset:3072
	v_lshl_add_u64 v[206:207], s[22:23], 0, v[134:135]
	s_add_i32 m0, s59, 0xc000
	ds_read_b128 v[170:173], v177
	ds_read_b128 v[178:181], v177 offset:1024
	ds_read_b128 v[182:185], v177 offset:2048
	ds_read_b128 v[186:189], v177 offset:3072
	ds_read_b128 v[190:193], v177 offset:4096
	ds_read_b128 v[194:197], v177 offset:5120
	ds_read_b128 v[198:201], v177 offset:6144
	ds_read_b128 v[202:205], v177 offset:7168
	global_load_lds_dwordx4 v[206:207], off
	v_lshl_add_u64 v[206:207], v[206:207], 0, s[12:13]
	s_add_i32 m0, s59, 0xe000
	s_nop 0
	global_load_lds_dwordx4 v[206:207], off
	s_waitcnt vmcnt(8)
	s_waitcnt lgkmcnt(0)
	s_barrier
	s_setprio 1
	v_mfma_f32_16x16x32_bf16 v[108:111], v[136:139], v[170:173], v[108:111]
	v_mfma_f32_16x16x32_bf16 v[104:107], v[144:147], v[170:173], v[104:107]
	v_mfma_f32_16x16x32_bf16 v[100:103], v[136:139], v[182:185], v[100:103]
	v_mfma_f32_16x16x32_bf16 v[96:99], v[144:147], v[182:185], v[96:99]
	v_mfma_f32_16x16x32_bf16 v[92:95], v[136:139], v[190:193], v[92:95]
	v_mfma_f32_16x16x32_bf16 v[88:91], v[144:147], v[190:193], v[88:91]
	v_mfma_f32_16x16x32_bf16 v[84:87], v[136:139], v[198:201], v[84:87]
	v_mfma_f32_16x16x32_bf16 v[80:83], v[144:147], v[198:201], v[80:83]
	v_mfma_f32_16x16x32_bf16 v[108:111], v[140:143], v[178:181], v[108:111]
	v_mfma_f32_16x16x32_bf16 v[104:107], v[148:151], v[178:181], v[104:107]
	v_mfma_f32_16x16x32_bf16 v[100:103], v[140:143], v[186:189], v[100:103]
	v_mfma_f32_16x16x32_bf16 v[96:99], v[148:151], v[186:189], v[96:99]
	v_mfma_f32_16x16x32_bf16 v[92:95], v[140:143], v[194:197], v[92:95]
	v_mfma_f32_16x16x32_bf16 v[88:91], v[148:151], v[194:197], v[88:91]
	v_mfma_f32_16x16x32_bf16 v[84:87], v[140:143], v[202:205], v[84:87]
	v_mfma_f32_16x16x32_bf16 v[80:83], v[148:151], v[202:205], v[80:83]
	v_mfma_f32_16x16x32_bf16 v[76:79], v[152:155], v[170:173], v[76:79]
	v_mfma_f32_16x16x32_bf16 v[72:75], v[162:165], v[170:173], v[72:75]
	v_mfma_f32_16x16x32_bf16 v[68:71], v[152:155], v[182:185], v[68:71]
	v_mfma_f32_16x16x32_bf16 v[64:67], v[162:165], v[182:185], v[64:67]
	v_mfma_f32_16x16x32_bf16 v[60:63], v[152:155], v[190:193], v[60:63]
	v_mfma_f32_16x16x32_bf16 v[56:59], v[162:165], v[190:193], v[56:59]
	v_mfma_f32_16x16x32_bf16 v[52:55], v[152:155], v[198:201], v[52:55]
	v_mfma_f32_16x16x32_bf16 v[48:51], v[162:165], v[198:201], v[48:51]
	v_mfma_f32_16x16x32_bf16 v[76:79], v[156:159], v[178:181], v[76:79]
	v_mfma_f32_16x16x32_bf16 v[72:75], v[166:169], v[178:181], v[72:75]
	v_mfma_f32_16x16x32_bf16 v[68:71], v[156:159], v[186:189], v[68:71]
	v_mfma_f32_16x16x32_bf16 v[64:67], v[166:169], v[186:189], v[64:67]
	v_mfma_f32_16x16x32_bf16 v[60:63], v[156:159], v[194:197], v[60:63]
	v_mfma_f32_16x16x32_bf16 v[56:59], v[166:169], v[194:197], v[56:59]
	v_mfma_f32_16x16x32_bf16 v[52:55], v[156:159], v[202:205], v[52:55]
	v_mfma_f32_16x16x32_bf16 v[48:51], v[166:169], v[202:205], v[48:51]
	s_setprio 0
	s_barrier
	v_lshl_add_u64 v[206:207], s[46:47], 0, v[128:129]
	s_add_i32 s46, s55, s58
	s_mov_b32 m0, s46
	ds_read_b128 v[170:173], v177 offset:16384
	ds_read_b128 v[178:181], v177 offset:17408
	ds_read_b128 v[182:185], v177 offset:18432
	ds_read_b128 v[186:189], v177 offset:19456
	ds_read_b128 v[190:193], v177 offset:20480
	ds_read_b128 v[194:197], v177 offset:21504
	ds_read_b128 v[198:201], v177 offset:22528
	ds_read_b128 v[202:205], v177 offset:23552
	global_load_lds_dwordx4 v[206:207], off
	v_lshl_add_u64 v[208:209], v[206:207], 0, s[8:9]
	s_add_i32 m0, s46, 0x2000
	s_add_i32 s46, s90, s58
	global_load_lds_dwordx4 v[208:209], off
	v_lshl_add_u64 v[208:209], v[206:207], 0, s[14:15]
	s_mov_b32 m0, s46
	s_nop 0
	global_load_lds_dwordx4 v[208:209], off
	v_lshl_add_u64 v[208:209], v[206:207], 0, s[16:17]
	s_add_i32 m0, s46, 0x2000
	s_nop 0
	global_load_lds_dwordx4 v[208:209], off
	v_lshl_add_u64 v[208:209], s[2:3], 0, v[130:131]
	s_mov_b32 m0, s59
	v_lshl_add_u64 v[210:211], v[208:209], 0, s[12:13]
	global_load_lds_dwordx4 v[208:209], off
	s_mov_b32 m0, s63
	s_nop 0
	global_load_lds_dwordx4 v[210:211], off
	s_waitcnt vmcnt(8)
	s_waitcnt lgkmcnt(0)
	s_barrier
	s_setprio 1
	v_mfma_f32_16x16x32_bf16 v[44:47], v[136:139], v[170:173], v[44:47]
	v_mfma_f32_16x16x32_bf16 v[40:43], v[144:147], v[170:173], v[40:43]
	v_mfma_f32_16x16x32_bf16 v[36:39], v[136:139], v[182:185], v[36:39]
	v_mfma_f32_16x16x32_bf16 v[32:35], v[144:147], v[182:185], v[32:35]
	v_mfma_f32_16x16x32_bf16 v[28:31], v[136:139], v[190:193], v[28:31]
	v_mfma_f32_16x16x32_bf16 v[24:27], v[144:147], v[190:193], v[24:27]
	v_mfma_f32_16x16x32_bf16 v[20:23], v[136:139], v[198:201], v[20:23]
	v_mfma_f32_16x16x32_bf16 v[16:19], v[144:147], v[198:201], v[16:19]
	v_mfma_f32_16x16x32_bf16 v[44:47], v[140:143], v[178:181], v[44:47]
	v_mfma_f32_16x16x32_bf16 v[40:43], v[148:151], v[178:181], v[40:43]
	v_mfma_f32_16x16x32_bf16 v[36:39], v[140:143], v[186:189], v[36:39]
	v_mfma_f32_16x16x32_bf16 v[32:35], v[148:151], v[186:189], v[32:35]
	v_mfma_f32_16x16x32_bf16 v[28:31], v[140:143], v[194:197], v[28:31]
	v_mfma_f32_16x16x32_bf16 v[24:27], v[148:151], v[194:197], v[24:27]
	v_mfma_f32_16x16x32_bf16 v[20:23], v[140:143], v[202:205], v[20:23]
	v_mfma_f32_16x16x32_bf16 v[16:19], v[148:151], v[202:205], v[16:19]
	v_mfma_f32_16x16x32_bf16 v[12:15], v[152:155], v[170:173], v[12:15]
	v_mfma_f32_16x16x32_bf16 v[8:11], v[162:165], v[170:173], v[8:11]
	v_mfma_f32_16x16x32_bf16 v[4:7], v[152:155], v[182:185], v[4:7]
	v_mfma_f32_16x16x32_bf16 v[0:3], v[162:165], v[182:185], v[0:3]
	v_mfma_f32_16x16x32_bf16 v[112:115], v[152:155], v[190:193], v[112:115]
	v_mfma_f32_16x16x32_bf16 v[116:119], v[162:165], v[190:193], v[116:119]
	v_mfma_f32_16x16x32_bf16 v[120:123], v[152:155], v[198:201], v[120:123]
	v_mfma_f32_16x16x32_bf16 v[124:127], v[162:165], v[198:201], v[124:127]
	v_mfma_f32_16x16x32_bf16 v[12:15], v[156:159], v[178:181], v[12:15]
	v_mfma_f32_16x16x32_bf16 v[8:11], v[166:169], v[178:181], v[8:11]
	v_mfma_f32_16x16x32_bf16 v[4:7], v[156:159], v[186:189], v[4:7]
	v_mfma_f32_16x16x32_bf16 v[0:3], v[166:169], v[186:189], v[0:3]
	v_mfma_f32_16x16x32_bf16 v[112:115], v[156:159], v[194:197], v[112:115]
	v_mfma_f32_16x16x32_bf16 v[116:119], v[166:169], v[194:197], v[116:119]
	v_mfma_f32_16x16x32_bf16 v[120:123], v[156:159], v[202:205], v[120:123]
	v_mfma_f32_16x16x32_bf16 v[124:127], v[166:169], v[202:205], v[124:127]
	s_setprio 0
	s_barrier
	s_add_i32 s2, 0, 0x18000
	s_add_i32 s3, 0, 0x1c000
	v_add_u32_e32 v148, s2, v175
	v_add_u32_e32 v160, s3, v175
	ds_read_b128 v[136:139], v148
	ds_read_b128 v[140:143], v148 offset:1024
	ds_read_b128 v[144:147], v148 offset:2048
	ds_read_b128 v[148:151], v148 offset:3072
	ds_read_b128 v[152:155], v160
	ds_read_b128 v[156:159], v160 offset:1024
	ds_read_b128 v[162:165], v160 offset:2048
	ds_read_b128 v[166:169], v160 offset:3072
	s_mov_b32 m0, s77
	v_lshl_add_u64 v[210:211], v[208:209], 0, s[4:5]
	ds_read_b128 v[170:173], v177 offset:32768
	ds_read_b128 v[178:181], v177 offset:33792
	ds_read_b128 v[182:185], v177 offset:34816
	ds_read_b128 v[186:189], v177 offset:35840
	ds_read_b128 v[190:193], v177 offset:36864
	ds_read_b128 v[194:197], v177 offset:37888
	ds_read_b128 v[198:201], v177 offset:38912
	ds_read_b128 v[202:205], v177 offset:39936
	global_load_lds_dwordx4 v[210:211], off
	v_lshl_add_u64 v[210:211], v[208:209], 0, s[72:73]
	s_mov_b32 m0, s78
	s_nop 0
	global_load_lds_dwordx4 v[210:211], off
	s_waitcnt vmcnt(8)
	s_waitcnt lgkmcnt(0)
	s_barrier
	s_setprio 1
	v_mfma_f32_16x16x32_bf16 v[108:111], v[136:139], v[170:173], v[108:111]
	v_mfma_f32_16x16x32_bf16 v[104:107], v[144:147], v[170:173], v[104:107]
	v_mfma_f32_16x16x32_bf16 v[100:103], v[136:139], v[182:185], v[100:103]
	v_mfma_f32_16x16x32_bf16 v[96:99], v[144:147], v[182:185], v[96:99]
	v_mfma_f32_16x16x32_bf16 v[92:95], v[136:139], v[190:193], v[92:95]
	v_mfma_f32_16x16x32_bf16 v[88:91], v[144:147], v[190:193], v[88:91]
	v_mfma_f32_16x16x32_bf16 v[84:87], v[136:139], v[198:201], v[84:87]
	v_mfma_f32_16x16x32_bf16 v[80:83], v[144:147], v[198:201], v[80:83]
	v_mfma_f32_16x16x32_bf16 v[108:111], v[140:143], v[178:181], v[108:111]
	v_mfma_f32_16x16x32_bf16 v[104:107], v[148:151], v[178:181], v[104:107]
	v_mfma_f32_16x16x32_bf16 v[100:103], v[140:143], v[186:189], v[100:103]
	v_mfma_f32_16x16x32_bf16 v[96:99], v[148:151], v[186:189], v[96:99]
	v_mfma_f32_16x16x32_bf16 v[92:95], v[140:143], v[194:197], v[92:95]
	v_mfma_f32_16x16x32_bf16 v[88:91], v[148:151], v[194:197], v[88:91]
	v_mfma_f32_16x16x32_bf16 v[84:87], v[140:143], v[202:205], v[84:87]
	v_mfma_f32_16x16x32_bf16 v[80:83], v[148:151], v[202:205], v[80:83]
	v_mfma_f32_16x16x32_bf16 v[76:79], v[152:155], v[170:173], v[76:79]
	v_mfma_f32_16x16x32_bf16 v[72:75], v[162:165], v[170:173], v[72:75]
	v_mfma_f32_16x16x32_bf16 v[68:71], v[152:155], v[182:185], v[68:71]
	v_mfma_f32_16x16x32_bf16 v[64:67], v[162:165], v[182:185], v[64:67]
	v_mfma_f32_16x16x32_bf16 v[60:63], v[152:155], v[190:193], v[60:63]
	v_mfma_f32_16x16x32_bf16 v[56:59], v[162:165], v[190:193], v[56:59]
	v_mfma_f32_16x16x32_bf16 v[52:55], v[152:155], v[198:201], v[52:55]
	v_mfma_f32_16x16x32_bf16 v[48:51], v[162:165], v[198:201], v[48:51]
	v_mfma_f32_16x16x32_bf16 v[76:79], v[156:159], v[178:181], v[76:79]
	v_mfma_f32_16x16x32_bf16 v[72:75], v[166:169], v[178:181], v[72:75]
	v_mfma_f32_16x16x32_bf16 v[68:71], v[156:159], v[186:189], v[68:71]
	v_mfma_f32_16x16x32_bf16 v[64:67], v[166:169], v[186:189], v[64:67]
	v_mfma_f32_16x16x32_bf16 v[60:63], v[156:159], v[194:197], v[60:63]
	v_mfma_f32_16x16x32_bf16 v[56:59], v[166:169], v[194:197], v[56:59]
	v_mfma_f32_16x16x32_bf16 v[52:55], v[156:159], v[202:205], v[52:55]
	v_mfma_f32_16x16x32_bf16 v[48:51], v[166:169], v[202:205], v[48:51]
	s_setprio 0
	s_barrier
	s_add_i32 s2, s2, s58
	v_lshl_add_u64 v[210:211], v[206:207], 0, s[56:57]
	s_mov_b32 m0, s2
	ds_read_b128 v[170:173], v177 offset:49152
	ds_read_b128 v[178:181], v177 offset:50176
	ds_read_b128 v[182:185], v177 offset:51200
	ds_read_b128 v[186:189], v177 offset:52224
	ds_read_b128 v[190:193], v177 offset:53248
	ds_read_b128 v[194:197], v177 offset:54272
	ds_read_b128 v[198:201], v177 offset:55296
	ds_read_b128 v[202:205], v177 offset:56320
	global_load_lds_dwordx4 v[210:211], off
	v_lshl_add_u64 v[210:211], v[206:207], 0, s[28:29]
	s_add_i32 m0, s2, 0x2000
	s_add_i32 s2, s3, s58
	global_load_lds_dwordx4 v[210:211], off
	v_lshl_add_u64 v[210:211], v[206:207], 0, s[0:1]
	s_mov_b32 m0, s2
	v_lshl_add_u64 v[206:207], v[206:207], 0, s[64:65]
	global_load_lds_dwordx4 v[210:211], off
	s_add_i32 m0, s2, 0x2000
	s_nop 0
	global_load_lds_dwordx4 v[206:207], off
	v_lshl_add_u64 v[206:207], v[208:209], 0, s[56:57]
	s_mov_b32 m0, s79
	s_nop 0
	global_load_lds_dwordx4 v[206:207], off
	v_lshl_add_u64 v[206:207], v[208:209], 0, s[88:89]
	s_mov_b32 m0, s10
	s_nop 0
	global_load_lds_dwordx4 v[206:207], off
	s_waitcnt vmcnt(8)
	s_waitcnt lgkmcnt(0)
	s_barrier
	s_setprio 1
	v_mfma_f32_16x16x32_bf16 v[44:47], v[136:139], v[170:173], v[44:47]
	v_mfma_f32_16x16x32_bf16 v[40:43], v[144:147], v[170:173], v[40:43]
	v_mfma_f32_16x16x32_bf16 v[36:39], v[136:139], v[182:185], v[36:39]
	v_mfma_f32_16x16x32_bf16 v[32:35], v[144:147], v[182:185], v[32:35]
	v_mfma_f32_16x16x32_bf16 v[28:31], v[136:139], v[190:193], v[28:31]
	v_mfma_f32_16x16x32_bf16 v[24:27], v[144:147], v[190:193], v[24:27]
	v_mfma_f32_16x16x32_bf16 v[20:23], v[136:139], v[198:201], v[20:23]
	v_mfma_f32_16x16x32_bf16 v[16:19], v[144:147], v[198:201], v[16:19]
	v_mfma_f32_16x16x32_bf16 v[44:47], v[140:143], v[178:181], v[44:47]
	v_mfma_f32_16x16x32_bf16 v[40:43], v[148:151], v[178:181], v[40:43]
	v_mfma_f32_16x16x32_bf16 v[36:39], v[140:143], v[186:189], v[36:39]
	v_mfma_f32_16x16x32_bf16 v[32:35], v[148:151], v[186:189], v[32:35]
	v_mfma_f32_16x16x32_bf16 v[28:31], v[140:143], v[194:197], v[28:31]
	v_mfma_f32_16x16x32_bf16 v[24:27], v[148:151], v[194:197], v[24:27]
	v_mfma_f32_16x16x32_bf16 v[20:23], v[140:143], v[202:205], v[20:23]
	v_mfma_f32_16x16x32_bf16 v[16:19], v[148:151], v[202:205], v[16:19]
	v_mfma_f32_16x16x32_bf16 v[12:15], v[152:155], v[170:173], v[12:15]
	v_mfma_f32_16x16x32_bf16 v[8:11], v[162:165], v[170:173], v[8:11]
	v_mfma_f32_16x16x32_bf16 v[4:7], v[152:155], v[182:185], v[4:7]
	v_mfma_f32_16x16x32_bf16 v[0:3], v[162:165], v[182:185], v[0:3]
	v_mfma_f32_16x16x32_bf16 v[112:115], v[152:155], v[190:193], v[112:115]
	v_mfma_f32_16x16x32_bf16 v[116:119], v[162:165], v[190:193], v[116:119]
	v_mfma_f32_16x16x32_bf16 v[120:123], v[152:155], v[198:201], v[120:123]
	v_mfma_f32_16x16x32_bf16 v[124:127], v[162:165], v[198:201], v[124:127]
	v_mfma_f32_16x16x32_bf16 v[12:15], v[156:159], v[178:181], v[12:15]
	v_mfma_f32_16x16x32_bf16 v[8:11], v[166:169], v[178:181], v[8:11]
	v_mfma_f32_16x16x32_bf16 v[4:7], v[156:159], v[186:189], v[4:7]
	v_mfma_f32_16x16x32_bf16 v[0:3], v[166:169], v[186:189], v[0:3]
	v_mfma_f32_16x16x32_bf16 v[112:115], v[156:159], v[194:197], v[112:115]
	v_mfma_f32_16x16x32_bf16 v[116:119], v[166:169], v[194:197], v[116:119]
	v_mfma_f32_16x16x32_bf16 v[120:123], v[156:159], v[202:205], v[120:123]
	v_mfma_f32_16x16x32_bf16 v[124:127], v[166:169], v[202:205], v[124:127]
	s_setprio 0
	s_barrier
	s_add_u32 s22, s22, 0x100
	s_addc_u32 s23, s23, 0
	s_add_u32 s43, s43, 0x100
	s_addc_u32 s44, s44, 0
	s_cmp_ge_i32 s45, s11
	s_mov_b32 s2, s45
	s_cbranch_scc0 .LBB0_865

.LBB0_1071:
	s_add_i32 s86, s2, 2
	s_add_u32 s87, s74, 0xfffc0080
	s_addc_u32 s3, s75, -1
	s_cmp_eq_u32 s80, s2
	s_cselect_b32 s3, s19, s3
	s_cselect_b32 s2, s38, s87
	s_cselect_b32 s91, s39, s23
	s_cselect_b32 s90, s49, s22
	s_add_i32 s87, 0, 0x10000
	s_add_i32 s92, 0, 0x14000
	v_add_u32_e32 v142, s87, v153
	v_add_u32_e32 v150, s92, v153
	ds_read_b128 v[130:133], v142
	ds_read_b128 v[134:137], v142 offset:1024
	ds_read_b128 v[138:141], v142 offset:2048
	ds_read_b128 v[142:145], v142 offset:3072
	ds_read_b128 v[146:149], v150
	ds_read_b128 v[156:159], v150 offset:1024
	ds_read_b128 v[162:165], v150 offset:2048
	ds_read_b128 v[166:169], v150 offset:3072
	v_lshl_add_u64 v[150:151], s[74:75], 0, v[128:129]
	s_add_i32 m0, s7, 0xc000
	ds_read_b128 v[170:173], v155
	ds_read_b128 v[174:177], v155 offset:1024
	ds_read_b128 v[178:181], v155 offset:2048
	ds_read_b128 v[182:185], v155 offset:3072
	ds_read_b128 v[186:189], v155 offset:4096
	ds_read_b128 v[190:193], v155 offset:5120
	ds_read_b128 v[194:197], v155 offset:6144
	ds_read_b128 v[198:201], v155 offset:7168
	global_load_lds_dwordx4 v[150:151], off
	v_lshl_add_u64 v[150:151], v[150:151], 0, s[14:15]
	s_add_i32 m0, s7, 0xe000
	s_nop 0
	global_load_lds_dwordx4 v[150:151], off
	s_waitcnt vmcnt(8)
	s_waitcnt lgkmcnt(0)
	s_barrier
	s_setprio 1
	v_mfma_f32_16x16x32_bf16 v[124:127], v[130:133], v[170:173], v[124:127]
	v_mfma_f32_16x16x32_bf16 v[120:123], v[138:141], v[170:173], v[120:123]
	v_mfma_f32_16x16x32_bf16 v[108:111], v[130:133], v[178:181], v[108:111]
	v_mfma_f32_16x16x32_bf16 v[104:107], v[138:141], v[178:181], v[104:107]
	v_mfma_f32_16x16x32_bf16 v[92:95], v[130:133], v[186:189], v[92:95]
	v_mfma_f32_16x16x32_bf16 v[88:91], v[138:141], v[186:189], v[88:91]
	v_mfma_f32_16x16x32_bf16 v[76:79], v[130:133], v[194:197], v[76:79]
	v_mfma_f32_16x16x32_bf16 v[72:75], v[138:141], v[194:197], v[72:75]
	v_mfma_f32_16x16x32_bf16 v[124:127], v[134:137], v[174:177], v[124:127]
	v_mfma_f32_16x16x32_bf16 v[120:123], v[142:145], v[174:177], v[120:123]
	v_mfma_f32_16x16x32_bf16 v[108:111], v[134:137], v[182:185], v[108:111]
	v_mfma_f32_16x16x32_bf16 v[104:107], v[142:145], v[182:185], v[104:107]
	v_mfma_f32_16x16x32_bf16 v[92:95], v[134:137], v[190:193], v[92:95]
	v_mfma_f32_16x16x32_bf16 v[88:91], v[142:145], v[190:193], v[88:91]
	v_mfma_f32_16x16x32_bf16 v[76:79], v[134:137], v[198:201], v[76:79]
	v_mfma_f32_16x16x32_bf16 v[72:75], v[142:145], v[198:201], v[72:75]
	v_mfma_f32_16x16x32_bf16 v[116:119], v[146:149], v[170:173], v[116:119]
	v_mfma_f32_16x16x32_bf16 v[112:115], v[162:165], v[170:173], v[112:115]
	v_mfma_f32_16x16x32_bf16 v[100:103], v[146:149], v[178:181], v[100:103]
	v_mfma_f32_16x16x32_bf16 v[96:99], v[162:165], v[178:181], v[96:99]
	v_mfma_f32_16x16x32_bf16 v[84:87], v[146:149], v[186:189], v[84:87]
	v_mfma_f32_16x16x32_bf16 v[80:83], v[162:165], v[186:189], v[80:83]
	v_mfma_f32_16x16x32_bf16 v[68:71], v[146:149], v[194:197], v[68:71]
	v_mfma_f32_16x16x32_bf16 v[64:67], v[162:165], v[194:197], v[64:67]
	v_mfma_f32_16x16x32_bf16 v[116:119], v[156:159], v[174:177], v[116:119]
	v_mfma_f32_16x16x32_bf16 v[112:115], v[166:169], v[174:177], v[112:115]
	v_mfma_f32_16x16x32_bf16 v[100:103], v[156:159], v[182:185], v[100:103]
	v_mfma_f32_16x16x32_bf16 v[96:99], v[166:169], v[182:185], v[96:99]
	v_mfma_f32_16x16x32_bf16 v[84:87], v[156:159], v[190:193], v[84:87]
	v_mfma_f32_16x16x32_bf16 v[80:83], v[166:169], v[190:193], v[80:83]
	v_mfma_f32_16x16x32_bf16 v[68:71], v[156:159], v[198:201], v[68:71]
	v_mfma_f32_16x16x32_bf16 v[64:67], v[166:169], v[198:201], v[64:67]
	s_setprio 0
	s_barrier
	s_add_i32 s87, s87, s6
	v_lshl_add_u64 v[150:151], s[90:91], 0, v[160:161]
	s_mov_b32 m0, s87
	ds_read_b128 v[170:173], v155 offset:16384
	ds_read_b128 v[174:177], v155 offset:17408
	ds_read_b128 v[178:181], v155 offset:18432
	ds_read_b128 v[182:185], v155 offset:19456
	ds_read_b128 v[186:189], v155 offset:20480
	ds_read_b128 v[190:193], v155 offset:21504
	ds_read_b128 v[194:197], v155 offset:22528
	ds_read_b128 v[198:201], v155 offset:23552
	global_load_lds_dwordx4 v[150:151], off
	v_lshl_add_u64 v[202:203], v[150:151], 0, s[14:15]
	s_add_i32 m0, s87, 0x2000
	s_add_i32 s87, s92, s6
	global_load_lds_dwordx4 v[202:203], off
	v_lshl_add_u64 v[202:203], v[150:151], 0, s[60:61]
	s_mov_b32 m0, s87
	s_nop 0
	global_load_lds_dwordx4 v[202:203], off
	v_lshl_add_u64 v[202:203], v[150:151], 0, s[52:53]
	s_add_i32 m0, s87, 0x2000
	s_nop 0
	global_load_lds_dwordx4 v[202:203], off
	v_lshl_add_u64 v[202:203], s[2:3], 0, v[160:161]
	s_mov_b32 m0, s7
	v_lshl_add_u64 v[204:205], v[202:203], 0, s[14:15]
	global_load_lds_dwordx4 v[202:203], off
	s_mov_b32 m0, s10
	s_nop 0
	global_load_lds_dwordx4 v[204:205], off
	s_waitcnt vmcnt(8)
	s_waitcnt lgkmcnt(0)
	s_barrier
	s_setprio 1
	v_mfma_f32_16x16x32_bf16 v[60:63], v[130:133], v[170:173], v[60:63]
	v_mfma_f32_16x16x32_bf16 v[56:59], v[138:141], v[170:173], v[56:59]
	v_mfma_f32_16x16x32_bf16 v[44:47], v[130:133], v[178:181], v[44:47]
	v_mfma_f32_16x16x32_bf16 v[40:43], v[138:141], v[178:181], v[40:43]
	v_mfma_f32_16x16x32_bf16 v[28:31], v[130:133], v[186:189], v[28:31]
	v_mfma_f32_16x16x32_bf16 v[24:27], v[138:141], v[186:189], v[24:27]
	v_mfma_f32_16x16x32_bf16 v[12:15], v[130:133], v[194:197], v[12:15]
	v_mfma_f32_16x16x32_bf16 v[8:11], v[138:141], v[194:197], v[8:11]
	v_mfma_f32_16x16x32_bf16 v[60:63], v[134:137], v[174:177], v[60:63]
	v_mfma_f32_16x16x32_bf16 v[56:59], v[142:145], v[174:177], v[56:59]
	v_mfma_f32_16x16x32_bf16 v[44:47], v[134:137], v[182:185], v[44:47]
	v_mfma_f32_16x16x32_bf16 v[40:43], v[142:145], v[182:185], v[40:43]
	v_mfma_f32_16x16x32_bf16 v[28:31], v[134:137], v[190:193], v[28:31]
	v_mfma_f32_16x16x32_bf16 v[24:27], v[142:145], v[190:193], v[24:27]
	v_mfma_f32_16x16x32_bf16 v[12:15], v[134:137], v[198:201], v[12:15]
	v_mfma_f32_16x16x32_bf16 v[8:11], v[142:145], v[198:201], v[8:11]
	v_mfma_f32_16x16x32_bf16 v[52:55], v[146:149], v[170:173], v[52:55]
	v_mfma_f32_16x16x32_bf16 v[48:51], v[162:165], v[170:173], v[48:51]
	v_mfma_f32_16x16x32_bf16 v[36:39], v[146:149], v[178:181], v[36:39]
	v_mfma_f32_16x16x32_bf16 v[32:35], v[162:165], v[178:181], v[32:35]
	v_mfma_f32_16x16x32_bf16 v[20:23], v[146:149], v[186:189], v[20:23]
	v_mfma_f32_16x16x32_bf16 v[16:19], v[162:165], v[186:189], v[16:19]
	v_mfma_f32_16x16x32_bf16 v[4:7], v[146:149], v[194:197], v[4:7]
	v_mfma_f32_16x16x32_bf16 v[0:3], v[162:165], v[194:197], v[0:3]
	v_mfma_f32_16x16x32_bf16 v[52:55], v[156:159], v[174:177], v[52:55]
	v_mfma_f32_16x16x32_bf16 v[48:51], v[166:169], v[174:177], v[48:51]
	v_mfma_f32_16x16x32_bf16 v[36:39], v[156:159], v[182:185], v[36:39]
	v_mfma_f32_16x16x32_bf16 v[32:35], v[166:169], v[182:185], v[32:35]
	v_mfma_f32_16x16x32_bf16 v[20:23], v[156:159], v[190:193], v[20:23]
	v_mfma_f32_16x16x32_bf16 v[16:19], v[166:169], v[190:193], v[16:19]
	v_mfma_f32_16x16x32_bf16 v[4:7], v[156:159], v[198:201], v[4:7]
	v_mfma_f32_16x16x32_bf16 v[0:3], v[166:169], v[198:201], v[0:3]
	s_setprio 0
	s_barrier
	s_add_i32 s2, 0, 0x18000
	s_add_i32 s3, 0, 0x1c000
	v_add_u32_e32 v142, s2, v153
	v_add_u32_e32 v166, s3, v153
	ds_read_b128 v[130:133], v142
	ds_read_b128 v[134:137], v142 offset:1024
	ds_read_b128 v[138:141], v142 offset:2048
	ds_read_b128 v[142:145], v142 offset:3072
	ds_read_b128 v[146:149], v166
	ds_read_b128 v[156:159], v166 offset:1024
	ds_read_b128 v[162:165], v166 offset:2048
	ds_read_b128 v[166:169], v166 offset:3072
	s_mov_b32 m0, s11
	v_lshl_add_u64 v[204:205], v[202:203], 0, s[60:61]
	ds_read_b128 v[170:173], v155 offset:32768
	ds_read_b128 v[174:177], v155 offset:33792
	ds_read_b128 v[178:181], v155 offset:34816
	ds_read_b128 v[182:185], v155 offset:35840
	ds_read_b128 v[186:189], v155 offset:36864
	ds_read_b128 v[190:193], v155 offset:37888
	ds_read_b128 v[194:197], v155 offset:38912
	ds_read_b128 v[198:201], v155 offset:39936
	global_load_lds_dwordx4 v[204:205], off
	v_lshl_add_u64 v[204:205], v[202:203], 0, s[52:53]
	s_mov_b32 m0, s63
	s_nop 0
	global_load_lds_dwordx4 v[204:205], off
	s_waitcnt vmcnt(8)
	s_waitcnt lgkmcnt(0)
	s_barrier
	s_setprio 1
	v_mfma_f32_16x16x32_bf16 v[124:127], v[130:133], v[170:173], v[124:127]
	v_mfma_f32_16x16x32_bf16 v[120:123], v[138:141], v[170:173], v[120:123]
	v_mfma_f32_16x16x32_bf16 v[108:111], v[130:133], v[178:181], v[108:111]
	v_mfma_f32_16x16x32_bf16 v[104:107], v[138:141], v[178:181], v[104:107]
	v_mfma_f32_16x16x32_bf16 v[92:95], v[130:133], v[186:189], v[92:95]
	v_mfma_f32_16x16x32_bf16 v[88:91], v[138:141], v[186:189], v[88:91]
	v_mfma_f32_16x16x32_bf16 v[76:79], v[130:133], v[194:197], v[76:79]
	v_mfma_f32_16x16x32_bf16 v[72:75], v[138:141], v[194:197], v[72:75]
	v_mfma_f32_16x16x32_bf16 v[124:127], v[134:137], v[174:177], v[124:127]
	v_mfma_f32_16x16x32_bf16 v[120:123], v[142:145], v[174:177], v[120:123]
	v_mfma_f32_16x16x32_bf16 v[108:111], v[134:137], v[182:185], v[108:111]
	v_mfma_f32_16x16x32_bf16 v[104:107], v[142:145], v[182:185], v[104:107]
	v_mfma_f32_16x16x32_bf16 v[92:95], v[134:137], v[190:193], v[92:95]
	v_mfma_f32_16x16x32_bf16 v[88:91], v[142:145], v[190:193], v[88:91]
	v_mfma_f32_16x16x32_bf16 v[76:79], v[134:137], v[198:201], v[76:79]
	v_mfma_f32_16x16x32_bf16 v[72:75], v[142:145], v[198:201], v[72:75]
	v_mfma_f32_16x16x32_bf16 v[116:119], v[146:149], v[170:173], v[116:119]
	v_mfma_f32_16x16x32_bf16 v[112:115], v[162:165], v[170:173], v[112:115]
	v_mfma_f32_16x16x32_bf16 v[100:103], v[146:149], v[178:181], v[100:103]
	v_mfma_f32_16x16x32_bf16 v[96:99], v[162:165], v[178:181], v[96:99]
	v_mfma_f32_16x16x32_bf16 v[84:87], v[146:149], v[186:189], v[84:87]
	v_mfma_f32_16x16x32_bf16 v[80:83], v[162:165], v[186:189], v[80:83]
	v_mfma_f32_16x16x32_bf16 v[68:71], v[146:149], v[194:197], v[68:71]
	v_mfma_f32_16x16x32_bf16 v[64:67], v[162:165], v[194:197], v[64:67]
	v_mfma_f32_16x16x32_bf16 v[116:119], v[156:159], v[174:177], v[116:119]
	v_mfma_f32_16x16x32_bf16 v[112:115], v[166:169], v[174:177], v[112:115]
	v_mfma_f32_16x16x32_bf16 v[100:103], v[156:159], v[182:185], v[100:103]
	v_mfma_f32_16x16x32_bf16 v[96:99], v[166:169], v[182:185], v[96:99]
	v_mfma_f32_16x16x32_bf16 v[84:87], v[156:159], v[190:193], v[84:87]
	v_mfma_f32_16x16x32_bf16 v[80:83], v[166:169], v[190:193], v[80:83]
	v_mfma_f32_16x16x32_bf16 v[68:71], v[156:159], v[198:201], v[68:71]
	v_mfma_f32_16x16x32_bf16 v[64:67], v[166:169], v[198:201], v[64:67]
	s_setprio 0
	s_barrier
	s_add_i32 s2, s2, s6
	v_lshl_add_u64 v[204:205], v[150:151], 0, s[56:57]
	s_mov_b32 m0, s2
	ds_read_b128 v[170:173], v155 offset:49152
	ds_read_b128 v[174:177], v155 offset:50176
	ds_read_b128 v[178:181], v155 offset:51200
	ds_read_b128 v[182:185], v155 offset:52224
	ds_read_b128 v[186:189], v155 offset:53248
	ds_read_b128 v[190:193], v155 offset:54272
	ds_read_b128 v[194:197], v155 offset:55296
	ds_read_b128 v[198:201], v155 offset:56320
	global_load_lds_dwordx4 v[204:205], off
	v_lshl_add_u64 v[204:205], v[150:151], 0, s[0:1]
	s_add_i32 m0, s2, 0x2000
	s_add_i32 s2, s3, s6
	global_load_lds_dwordx4 v[204:205], off
	v_lshl_add_u64 v[204:205], v[150:151], 0, s[24:25]
	s_mov_b32 m0, s2
	v_lshl_add_u64 v[150:151], v[150:151], 0, s[26:27]
	global_load_lds_dwordx4 v[204:205], off
	s_add_i32 m0, s2, 0x2000
	s_nop 0
	global_load_lds_dwordx4 v[150:151], off
	v_lshl_add_u64 v[150:151], v[202:203], 0, s[56:57]
	s_mov_b32 m0, s77
	s_nop 0
	global_load_lds_dwordx4 v[150:151], off
	v_lshl_add_u64 v[150:151], v[202:203], 0, s[0:1]
	s_mov_b32 m0, s78
	s_nop 0
	global_load_lds_dwordx4 v[150:151], off
	s_waitcnt vmcnt(8)
	s_waitcnt lgkmcnt(0)
	s_barrier
	s_setprio 1
	v_mfma_f32_16x16x32_bf16 v[60:63], v[130:133], v[170:173], v[60:63]
	v_mfma_f32_16x16x32_bf16 v[56:59], v[138:141], v[170:173], v[56:59]
	v_mfma_f32_16x16x32_bf16 v[44:47], v[130:133], v[178:181], v[44:47]
	v_mfma_f32_16x16x32_bf16 v[40:43], v[138:141], v[178:181], v[40:43]
	v_mfma_f32_16x16x32_bf16 v[28:31], v[130:133], v[186:189], v[28:31]
	v_mfma_f32_16x16x32_bf16 v[24:27], v[138:141], v[186:189], v[24:27]
	v_mfma_f32_16x16x32_bf16 v[12:15], v[130:133], v[194:197], v[12:15]
	v_mfma_f32_16x16x32_bf16 v[8:11], v[138:141], v[194:197], v[8:11]
	v_mfma_f32_16x16x32_bf16 v[60:63], v[134:137], v[174:177], v[60:63]
	v_mfma_f32_16x16x32_bf16 v[56:59], v[142:145], v[174:177], v[56:59]
	v_mfma_f32_16x16x32_bf16 v[44:47], v[134:137], v[182:185], v[44:47]
	v_mfma_f32_16x16x32_bf16 v[40:43], v[142:145], v[182:185], v[40:43]
	v_mfma_f32_16x16x32_bf16 v[28:31], v[134:137], v[190:193], v[28:31]
	v_mfma_f32_16x16x32_bf16 v[24:27], v[142:145], v[190:193], v[24:27]
	v_mfma_f32_16x16x32_bf16 v[12:15], v[134:137], v[198:201], v[12:15]
	v_mfma_f32_16x16x32_bf16 v[8:11], v[142:145], v[198:201], v[8:11]
	v_mfma_f32_16x16x32_bf16 v[52:55], v[146:149], v[170:173], v[52:55]
	v_mfma_f32_16x16x32_bf16 v[48:51], v[162:165], v[170:173], v[48:51]
	v_mfma_f32_16x16x32_bf16 v[36:39], v[146:149], v[178:181], v[36:39]
	v_mfma_f32_16x16x32_bf16 v[32:35], v[162:165], v[178:181], v[32:35]
	v_mfma_f32_16x16x32_bf16 v[20:23], v[146:149], v[186:189], v[20:23]
	v_mfma_f32_16x16x32_bf16 v[16:19], v[162:165], v[186:189], v[16:19]
	v_mfma_f32_16x16x32_bf16 v[4:7], v[146:149], v[194:197], v[4:7]
	v_mfma_f32_16x16x32_bf16 v[0:3], v[162:165], v[194:197], v[0:3]
	v_mfma_f32_16x16x32_bf16 v[52:55], v[156:159], v[174:177], v[52:55]
	v_mfma_f32_16x16x32_bf16 v[48:51], v[166:169], v[174:177], v[48:51]
	v_mfma_f32_16x16x32_bf16 v[36:39], v[156:159], v[182:185], v[36:39]
	v_mfma_f32_16x16x32_bf16 v[32:35], v[166:169], v[182:185], v[32:35]
	v_mfma_f32_16x16x32_bf16 v[20:23], v[156:159], v[190:193], v[20:23]
	v_mfma_f32_16x16x32_bf16 v[16:19], v[166:169], v[190:193], v[16:19]
	v_mfma_f32_16x16x32_bf16 v[4:7], v[156:159], v[198:201], v[4:7]
	v_mfma_f32_16x16x32_bf16 v[0:3], v[166:169], v[198:201], v[0:3]
	s_setprio 0
	s_barrier
	s_add_u32 s74, s74, 0x100
	s_addc_u32 s75, s75, 0
	s_add_u32 s22, s22, 0x100
	s_addc_u32 s23, s23, 0
	s_cmp_ge_i32 s86, s79
	s_mov_b32 s2, s86
	s_cbranch_scc0 .LBB0_1071

.LBB0_1094:
	s_add_i32 s86, s2, 2
	s_add_u32 s87, s74, 0xfffc0080
	s_addc_u32 s3, s75, -1
	s_cmp_eq_u32 s80, s2
	s_cselect_b32 s3, s38, s3
	s_cselect_b32 s2, s39, s87
	s_cselect_b32 s91, s47, s23
	s_cselect_b32 s90, s49, s22
	s_add_i32 s87, 0, 0x10000
	s_add_i32 s92, 0, 0x14000
	v_add_u32_e32 v146, s87, v135
	v_add_u32_e32 v158, s92, v135
	ds_read_b128 v[130:133], v146
	ds_read_b128 v[138:141], v146 offset:1024
	ds_read_b128 v[142:145], v146 offset:2048
	ds_read_b128 v[146:149], v146 offset:3072
	ds_read_b128 v[150:153], v158
	ds_read_b128 v[154:157], v158 offset:1024
	ds_read_b128 v[162:165], v158 offset:2048
	ds_read_b128 v[166:169], v158 offset:3072
	v_lshl_add_u64 v[158:159], s[74:75], 0, v[128:129]
	s_add_i32 m0, s7, 0xc000
	ds_read_b128 v[170:173], v137
	ds_read_b128 v[174:177], v137 offset:1024
	ds_read_b128 v[178:181], v137 offset:2048
	ds_read_b128 v[182:185], v137 offset:3072
	ds_read_b128 v[186:189], v137 offset:4096
	ds_read_b128 v[190:193], v137 offset:5120
	ds_read_b128 v[194:197], v137 offset:6144
	ds_read_b128 v[198:201], v137 offset:7168
	global_load_lds_dwordx4 v[158:159], off
	v_lshl_add_u64 v[158:159], v[158:159], 0, s[14:15]
	s_add_i32 m0, s7, 0xe000
	s_nop 0
	global_load_lds_dwordx4 v[158:159], off
	s_waitcnt vmcnt(8)
	s_waitcnt lgkmcnt(0)
	s_barrier
	s_setprio 1
	v_mfma_f32_16x16x32_bf16 v[124:127], v[130:133], v[170:173], v[124:127]
	v_mfma_f32_16x16x32_bf16 v[120:123], v[142:145], v[170:173], v[120:123]
	v_mfma_f32_16x16x32_bf16 v[108:111], v[130:133], v[178:181], v[108:111]
	v_mfma_f32_16x16x32_bf16 v[104:107], v[142:145], v[178:181], v[104:107]
	v_mfma_f32_16x16x32_bf16 v[92:95], v[130:133], v[186:189], v[92:95]
	v_mfma_f32_16x16x32_bf16 v[88:91], v[142:145], v[186:189], v[88:91]
	v_mfma_f32_16x16x32_bf16 v[76:79], v[130:133], v[194:197], v[76:79]
	v_mfma_f32_16x16x32_bf16 v[72:75], v[142:145], v[194:197], v[72:75]
	v_mfma_f32_16x16x32_bf16 v[124:127], v[138:141], v[174:177], v[124:127]
	v_mfma_f32_16x16x32_bf16 v[120:123], v[146:149], v[174:177], v[120:123]
	v_mfma_f32_16x16x32_bf16 v[108:111], v[138:141], v[182:185], v[108:111]
	v_mfma_f32_16x16x32_bf16 v[104:107], v[146:149], v[182:185], v[104:107]
	v_mfma_f32_16x16x32_bf16 v[92:95], v[138:141], v[190:193], v[92:95]
	v_mfma_f32_16x16x32_bf16 v[88:91], v[146:149], v[190:193], v[88:91]
	v_mfma_f32_16x16x32_bf16 v[76:79], v[138:141], v[198:201], v[76:79]
	v_mfma_f32_16x16x32_bf16 v[72:75], v[146:149], v[198:201], v[72:75]
	v_mfma_f32_16x16x32_bf16 v[116:119], v[150:153], v[170:173], v[116:119]
	v_mfma_f32_16x16x32_bf16 v[112:115], v[162:165], v[170:173], v[112:115]
	v_mfma_f32_16x16x32_bf16 v[100:103], v[150:153], v[178:181], v[100:103]
	v_mfma_f32_16x16x32_bf16 v[96:99], v[162:165], v[178:181], v[96:99]
	v_mfma_f32_16x16x32_bf16 v[84:87], v[150:153], v[186:189], v[84:87]
	v_mfma_f32_16x16x32_bf16 v[80:83], v[162:165], v[186:189], v[80:83]
	v_mfma_f32_16x16x32_bf16 v[68:71], v[150:153], v[194:197], v[68:71]
	v_mfma_f32_16x16x32_bf16 v[64:67], v[162:165], v[194:197], v[64:67]
	v_mfma_f32_16x16x32_bf16 v[116:119], v[154:157], v[174:177], v[116:119]
	v_mfma_f32_16x16x32_bf16 v[112:115], v[166:169], v[174:177], v[112:115]
	v_mfma_f32_16x16x32_bf16 v[100:103], v[154:157], v[182:185], v[100:103]
	v_mfma_f32_16x16x32_bf16 v[96:99], v[166:169], v[182:185], v[96:99]
	v_mfma_f32_16x16x32_bf16 v[84:87], v[154:157], v[190:193], v[84:87]
	v_mfma_f32_16x16x32_bf16 v[80:83], v[166:169], v[190:193], v[80:83]
	v_mfma_f32_16x16x32_bf16 v[68:71], v[154:157], v[198:201], v[68:71]
	v_mfma_f32_16x16x32_bf16 v[64:67], v[166:169], v[198:201], v[64:67]
	s_setprio 0
	s_barrier
	s_add_i32 s87, s87, s6
	v_lshl_add_u64 v[158:159], s[90:91], 0, v[160:161]
	s_mov_b32 m0, s87
	ds_read_b128 v[170:173], v137 offset:16384
	ds_read_b128 v[174:177], v137 offset:17408
	ds_read_b128 v[178:181], v137 offset:18432
	ds_read_b128 v[182:185], v137 offset:19456
	ds_read_b128 v[186:189], v137 offset:20480
	ds_read_b128 v[190:193], v137 offset:21504
	ds_read_b128 v[194:197], v137 offset:22528
	ds_read_b128 v[198:201], v137 offset:23552
	global_load_lds_dwordx4 v[158:159], off
	v_lshl_add_u64 v[202:203], v[158:159], 0, s[14:15]
	s_add_i32 m0, s87, 0x2000
	s_add_i32 s87, s92, s6
	global_load_lds_dwordx4 v[202:203], off
	v_lshl_add_u64 v[202:203], v[158:159], 0, s[60:61]
	s_mov_b32 m0, s87
	s_nop 0
	global_load_lds_dwordx4 v[202:203], off
	v_lshl_add_u64 v[202:203], v[158:159], 0, s[52:53]
	s_add_i32 m0, s87, 0x2000
	s_nop 0
	global_load_lds_dwordx4 v[202:203], off
	v_lshl_add_u64 v[202:203], s[2:3], 0, v[160:161]
	s_mov_b32 m0, s7
	v_lshl_add_u64 v[204:205], v[202:203], 0, s[14:15]
	global_load_lds_dwordx4 v[202:203], off
	s_mov_b32 m0, s10
	s_nop 0
	global_load_lds_dwordx4 v[204:205], off
	s_waitcnt vmcnt(8)
	s_waitcnt lgkmcnt(0)
	s_barrier
	s_setprio 1
	v_mfma_f32_16x16x32_bf16 v[60:63], v[130:133], v[170:173], v[60:63]
	v_mfma_f32_16x16x32_bf16 v[56:59], v[142:145], v[170:173], v[56:59]
	v_mfma_f32_16x16x32_bf16 v[44:47], v[130:133], v[178:181], v[44:47]
	v_mfma_f32_16x16x32_bf16 v[40:43], v[142:145], v[178:181], v[40:43]
	v_mfma_f32_16x16x32_bf16 v[28:31], v[130:133], v[186:189], v[28:31]
	v_mfma_f32_16x16x32_bf16 v[24:27], v[142:145], v[186:189], v[24:27]
	v_mfma_f32_16x16x32_bf16 v[12:15], v[130:133], v[194:197], v[12:15]
	v_mfma_f32_16x16x32_bf16 v[8:11], v[142:145], v[194:197], v[8:11]
	v_mfma_f32_16x16x32_bf16 v[60:63], v[138:141], v[174:177], v[60:63]
	v_mfma_f32_16x16x32_bf16 v[56:59], v[146:149], v[174:177], v[56:59]
	v_mfma_f32_16x16x32_bf16 v[44:47], v[138:141], v[182:185], v[44:47]
	v_mfma_f32_16x16x32_bf16 v[40:43], v[146:149], v[182:185], v[40:43]
	v_mfma_f32_16x16x32_bf16 v[28:31], v[138:141], v[190:193], v[28:31]
	v_mfma_f32_16x16x32_bf16 v[24:27], v[146:149], v[190:193], v[24:27]
	v_mfma_f32_16x16x32_bf16 v[12:15], v[138:141], v[198:201], v[12:15]
	v_mfma_f32_16x16x32_bf16 v[8:11], v[146:149], v[198:201], v[8:11]
	v_mfma_f32_16x16x32_bf16 v[52:55], v[150:153], v[170:173], v[52:55]
	v_mfma_f32_16x16x32_bf16 v[48:51], v[162:165], v[170:173], v[48:51]
	v_mfma_f32_16x16x32_bf16 v[36:39], v[150:153], v[178:181], v[36:39]
	v_mfma_f32_16x16x32_bf16 v[32:35], v[162:165], v[178:181], v[32:35]
	v_mfma_f32_16x16x32_bf16 v[20:23], v[150:153], v[186:189], v[20:23]
	v_mfma_f32_16x16x32_bf16 v[16:19], v[162:165], v[186:189], v[16:19]
	v_mfma_f32_16x16x32_bf16 v[4:7], v[150:153], v[194:197], v[4:7]
	v_mfma_f32_16x16x32_bf16 v[0:3], v[162:165], v[194:197], v[0:3]
	v_mfma_f32_16x16x32_bf16 v[52:55], v[154:157], v[174:177], v[52:55]
	v_mfma_f32_16x16x32_bf16 v[48:51], v[166:169], v[174:177], v[48:51]
	v_mfma_f32_16x16x32_bf16 v[36:39], v[154:157], v[182:185], v[36:39]
	v_mfma_f32_16x16x32_bf16 v[32:35], v[166:169], v[182:185], v[32:35]
	v_mfma_f32_16x16x32_bf16 v[20:23], v[154:157], v[190:193], v[20:23]
	v_mfma_f32_16x16x32_bf16 v[16:19], v[166:169], v[190:193], v[16:19]
	v_mfma_f32_16x16x32_bf16 v[4:7], v[154:157], v[198:201], v[4:7]
	v_mfma_f32_16x16x32_bf16 v[0:3], v[166:169], v[198:201], v[0:3]
	s_setprio 0
	s_barrier
	s_add_i32 s2, 0, 0x18000
	s_add_i32 s3, 0, 0x1c000
	v_add_u32_e32 v146, s2, v135
	v_add_u32_e32 v166, s3, v135
	ds_read_b128 v[130:133], v146
	ds_read_b128 v[138:141], v146 offset:1024
	ds_read_b128 v[142:145], v146 offset:2048
	ds_read_b128 v[146:149], v146 offset:3072
	ds_read_b128 v[150:153], v166
	ds_read_b128 v[154:157], v166 offset:1024
	ds_read_b128 v[162:165], v166 offset:2048
	ds_read_b128 v[166:169], v166 offset:3072
	s_mov_b32 m0, s11
	v_lshl_add_u64 v[204:205], v[202:203], 0, s[60:61]
	ds_read_b128 v[170:173], v137 offset:32768
	ds_read_b128 v[174:177], v137 offset:33792
	ds_read_b128 v[178:181], v137 offset:34816
	ds_read_b128 v[182:185], v137 offset:35840
	ds_read_b128 v[186:189], v137 offset:36864
	ds_read_b128 v[190:193], v137 offset:37888
	ds_read_b128 v[194:197], v137 offset:38912
	ds_read_b128 v[198:201], v137 offset:39936
	global_load_lds_dwordx4 v[204:205], off
	v_lshl_add_u64 v[204:205], v[202:203], 0, s[52:53]
	s_mov_b32 m0, s63
	s_nop 0
	global_load_lds_dwordx4 v[204:205], off
	s_waitcnt vmcnt(8)
	s_waitcnt lgkmcnt(0)
	s_barrier
	s_setprio 1
	v_mfma_f32_16x16x32_bf16 v[124:127], v[130:133], v[170:173], v[124:127]
	v_mfma_f32_16x16x32_bf16 v[120:123], v[142:145], v[170:173], v[120:123]
	v_mfma_f32_16x16x32_bf16 v[108:111], v[130:133], v[178:181], v[108:111]
	v_mfma_f32_16x16x32_bf16 v[104:107], v[142:145], v[178:181], v[104:107]
	v_mfma_f32_16x16x32_bf16 v[92:95], v[130:133], v[186:189], v[92:95]
	v_mfma_f32_16x16x32_bf16 v[88:91], v[142:145], v[186:189], v[88:91]
	v_mfma_f32_16x16x32_bf16 v[76:79], v[130:133], v[194:197], v[76:79]
	v_mfma_f32_16x16x32_bf16 v[72:75], v[142:145], v[194:197], v[72:75]
	v_mfma_f32_16x16x32_bf16 v[124:127], v[138:141], v[174:177], v[124:127]
	v_mfma_f32_16x16x32_bf16 v[120:123], v[146:149], v[174:177], v[120:123]
	v_mfma_f32_16x16x32_bf16 v[108:111], v[138:141], v[182:185], v[108:111]
	v_mfma_f32_16x16x32_bf16 v[104:107], v[146:149], v[182:185], v[104:107]
	v_mfma_f32_16x16x32_bf16 v[92:95], v[138:141], v[190:193], v[92:95]
	v_mfma_f32_16x16x32_bf16 v[88:91], v[146:149], v[190:193], v[88:91]
	v_mfma_f32_16x16x32_bf16 v[76:79], v[138:141], v[198:201], v[76:79]
	v_mfma_f32_16x16x32_bf16 v[72:75], v[146:149], v[198:201], v[72:75]
	v_mfma_f32_16x16x32_bf16 v[116:119], v[150:153], v[170:173], v[116:119]
	v_mfma_f32_16x16x32_bf16 v[112:115], v[162:165], v[170:173], v[112:115]
	v_mfma_f32_16x16x32_bf16 v[100:103], v[150:153], v[178:181], v[100:103]
	v_mfma_f32_16x16x32_bf16 v[96:99], v[162:165], v[178:181], v[96:99]
	v_mfma_f32_16x16x32_bf16 v[84:87], v[150:153], v[186:189], v[84:87]
	v_mfma_f32_16x16x32_bf16 v[80:83], v[162:165], v[186:189], v[80:83]
	v_mfma_f32_16x16x32_bf16 v[68:71], v[150:153], v[194:197], v[68:71]
	v_mfma_f32_16x16x32_bf16 v[64:67], v[162:165], v[194:197], v[64:67]
	v_mfma_f32_16x16x32_bf16 v[116:119], v[154:157], v[174:177], v[116:119]
	v_mfma_f32_16x16x32_bf16 v[112:115], v[166:169], v[174:177], v[112:115]
	v_mfma_f32_16x16x32_bf16 v[100:103], v[154:157], v[182:185], v[100:103]
	v_mfma_f32_16x16x32_bf16 v[96:99], v[166:169], v[182:185], v[96:99]
	v_mfma_f32_16x16x32_bf16 v[84:87], v[154:157], v[190:193], v[84:87]
	v_mfma_f32_16x16x32_bf16 v[80:83], v[166:169], v[190:193], v[80:83]
	v_mfma_f32_16x16x32_bf16 v[68:71], v[154:157], v[198:201], v[68:71]
	v_mfma_f32_16x16x32_bf16 v[64:67], v[166:169], v[198:201], v[64:67]
	s_setprio 0
	s_barrier
	s_add_i32 s2, s2, s6
	v_lshl_add_u64 v[204:205], v[158:159], 0, s[56:57]
	s_mov_b32 m0, s2
	ds_read_b128 v[170:173], v137 offset:49152
	ds_read_b128 v[174:177], v137 offset:50176
	ds_read_b128 v[178:181], v137 offset:51200
	ds_read_b128 v[182:185], v137 offset:52224
	ds_read_b128 v[186:189], v137 offset:53248
	ds_read_b128 v[190:193], v137 offset:54272
	ds_read_b128 v[194:197], v137 offset:55296
	ds_read_b128 v[198:201], v137 offset:56320
	global_load_lds_dwordx4 v[204:205], off
	v_lshl_add_u64 v[204:205], v[158:159], 0, s[0:1]
	s_add_i32 m0, s2, 0x2000
	s_add_i32 s2, s3, s6
	global_load_lds_dwordx4 v[204:205], off
	v_lshl_add_u64 v[204:205], v[158:159], 0, s[24:25]
	s_mov_b32 m0, s2
	v_lshl_add_u64 v[158:159], v[158:159], 0, s[26:27]
	global_load_lds_dwordx4 v[204:205], off
	s_add_i32 m0, s2, 0x2000
	s_nop 0
	global_load_lds_dwordx4 v[158:159], off
	v_lshl_add_u64 v[158:159], v[202:203], 0, s[56:57]
	s_mov_b32 m0, s77
	s_nop 0
	global_load_lds_dwordx4 v[158:159], off
	v_lshl_add_u64 v[158:159], v[202:203], 0, s[0:1]
	s_mov_b32 m0, s78
	s_nop 0
	global_load_lds_dwordx4 v[158:159], off
	s_waitcnt vmcnt(8)
	s_waitcnt lgkmcnt(0)
	s_barrier
	s_setprio 1
	v_mfma_f32_16x16x32_bf16 v[60:63], v[130:133], v[170:173], v[60:63]
	v_mfma_f32_16x16x32_bf16 v[56:59], v[142:145], v[170:173], v[56:59]
	v_mfma_f32_16x16x32_bf16 v[44:47], v[130:133], v[178:181], v[44:47]
	v_mfma_f32_16x16x32_bf16 v[40:43], v[142:145], v[178:181], v[40:43]
	v_mfma_f32_16x16x32_bf16 v[28:31], v[130:133], v[186:189], v[28:31]
	v_mfma_f32_16x16x32_bf16 v[24:27], v[142:145], v[186:189], v[24:27]
	v_mfma_f32_16x16x32_bf16 v[12:15], v[130:133], v[194:197], v[12:15]
	v_mfma_f32_16x16x32_bf16 v[8:11], v[142:145], v[194:197], v[8:11]
	v_mfma_f32_16x16x32_bf16 v[60:63], v[138:141], v[174:177], v[60:63]
	v_mfma_f32_16x16x32_bf16 v[56:59], v[146:149], v[174:177], v[56:59]
	v_mfma_f32_16x16x32_bf16 v[44:47], v[138:141], v[182:185], v[44:47]
	v_mfma_f32_16x16x32_bf16 v[40:43], v[146:149], v[182:185], v[40:43]
	v_mfma_f32_16x16x32_bf16 v[28:31], v[138:141], v[190:193], v[28:31]
	v_mfma_f32_16x16x32_bf16 v[24:27], v[146:149], v[190:193], v[24:27]
	v_mfma_f32_16x16x32_bf16 v[12:15], v[138:141], v[198:201], v[12:15]
	v_mfma_f32_16x16x32_bf16 v[8:11], v[146:149], v[198:201], v[8:11]
	v_mfma_f32_16x16x32_bf16 v[52:55], v[150:153], v[170:173], v[52:55]
	v_mfma_f32_16x16x32_bf16 v[48:51], v[162:165], v[170:173], v[48:51]
	v_mfma_f32_16x16x32_bf16 v[36:39], v[150:153], v[178:181], v[36:39]
	v_mfma_f32_16x16x32_bf16 v[32:35], v[162:165], v[178:181], v[32:35]
	v_mfma_f32_16x16x32_bf16 v[20:23], v[150:153], v[186:189], v[20:23]
	v_mfma_f32_16x16x32_bf16 v[16:19], v[162:165], v[186:189], v[16:19]
	v_mfma_f32_16x16x32_bf16 v[4:7], v[150:153], v[194:197], v[4:7]
	v_mfma_f32_16x16x32_bf16 v[0:3], v[162:165], v[194:197], v[0:3]
	v_mfma_f32_16x16x32_bf16 v[52:55], v[154:157], v[174:177], v[52:55]
	v_mfma_f32_16x16x32_bf16 v[48:51], v[166:169], v[174:177], v[48:51]
	v_mfma_f32_16x16x32_bf16 v[36:39], v[154:157], v[182:185], v[36:39]
	v_mfma_f32_16x16x32_bf16 v[32:35], v[166:169], v[182:185], v[32:35]
	v_mfma_f32_16x16x32_bf16 v[20:23], v[154:157], v[190:193], v[20:23]
	v_mfma_f32_16x16x32_bf16 v[16:19], v[166:169], v[190:193], v[16:19]
	v_mfma_f32_16x16x32_bf16 v[4:7], v[154:157], v[198:201], v[4:7]
	v_mfma_f32_16x16x32_bf16 v[0:3], v[166:169], v[198:201], v[0:3]
	s_setprio 0
	s_barrier
	s_add_u32 s74, s74, 0x100
	s_addc_u32 s75, s75, 0
	s_add_u32 s22, s22, 0x100
	s_addc_u32 s23, s23, 0
	s_cmp_ge_i32 s86, s79
	s_mov_b32 s2, s86
	s_cbranch_scc0 .LBB0_1094

.LBB0_1232:
	s_add_i32 s81, s2, 2
	s_add_u32 s83, s54, 0xfffc0080
	s_addc_u32 s3, s55, -1
	s_cmp_eq_u32 s78, s2
	s_cselect_b32 s3, s38, s3
	s_cselect_b32 s2, s39, s83
	s_cselect_b32 s87, s45, s23
	s_cselect_b32 s86, s47, s22
	s_add_i32 s83, 0, 0x10000
	v_add_u32_e32 v132, s83, v135
	s_add_i32 s90, 0, 0x14000
	ds_read_b128 v[138:141], v132
	ds_read_b128 v[142:145], v132 offset:1024
	ds_read_b128 v[146:149], v132 offset:2048
	ds_read_b128 v[150:153], v132 offset:3072
	v_add_u32_e32 v132, s90, v135
	ds_read_b128 v[154:157], v132
	ds_read_b128 v[162:165], v132 offset:1024
	ds_read_b128 v[166:169], v132 offset:2048
	ds_read_b128 v[170:173], v132 offset:3072
	v_lshl_add_u64 v[132:133], s[54:55], 0, v[130:131]
	s_add_i32 m0, s33, 0xc000
	ds_read_b128 v[174:177], v137
	ds_read_b128 v[178:181], v137 offset:1024
	ds_read_b128 v[182:185], v137 offset:2048
	ds_read_b128 v[186:189], v137 offset:3072
	ds_read_b128 v[190:193], v137 offset:4096
	ds_read_b128 v[194:197], v137 offset:5120
	ds_read_b128 v[198:201], v137 offset:6144
	ds_read_b128 v[202:205], v137 offset:7168
	global_load_lds_dwordx4 v[132:133], off
	v_lshl_add_u64 v[132:133], v[132:133], 0, s[14:15]
	s_add_i32 m0, s33, 0xe000
	s_nop 0
	global_load_lds_dwordx4 v[132:133], off
	s_waitcnt vmcnt(8)
	s_waitcnt lgkmcnt(0)
	s_barrier
	s_setprio 1
	v_mfma_f32_16x16x32_bf16 v[124:127], v[138:141], v[174:177], v[124:127]
	v_mfma_f32_16x16x32_bf16 v[116:119], v[146:149], v[174:177], v[116:119]
	v_mfma_f32_16x16x32_bf16 v[108:111], v[138:141], v[182:185], v[108:111]
	v_mfma_f32_16x16x32_bf16 v[100:103], v[146:149], v[182:185], v[100:103]
	v_mfma_f32_16x16x32_bf16 v[92:95], v[138:141], v[190:193], v[92:95]
	v_mfma_f32_16x16x32_bf16 v[84:87], v[146:149], v[190:193], v[84:87]
	v_mfma_f32_16x16x32_bf16 v[76:79], v[138:141], v[198:201], v[76:79]
	v_mfma_f32_16x16x32_bf16 v[68:71], v[146:149], v[198:201], v[68:71]
	v_mfma_f32_16x16x32_bf16 v[124:127], v[142:145], v[178:181], v[124:127]
	v_mfma_f32_16x16x32_bf16 v[116:119], v[150:153], v[178:181], v[116:119]
	v_mfma_f32_16x16x32_bf16 v[108:111], v[142:145], v[186:189], v[108:111]
	v_mfma_f32_16x16x32_bf16 v[100:103], v[150:153], v[186:189], v[100:103]
	v_mfma_f32_16x16x32_bf16 v[92:95], v[142:145], v[194:197], v[92:95]
	v_mfma_f32_16x16x32_bf16 v[84:87], v[150:153], v[194:197], v[84:87]
	v_mfma_f32_16x16x32_bf16 v[76:79], v[142:145], v[202:205], v[76:79]
	v_mfma_f32_16x16x32_bf16 v[68:71], v[150:153], v[202:205], v[68:71]
	v_mfma_f32_16x16x32_bf16 v[120:123], v[154:157], v[174:177], v[120:123]
	v_mfma_f32_16x16x32_bf16 v[112:115], v[166:169], v[174:177], v[112:115]
	v_mfma_f32_16x16x32_bf16 v[104:107], v[154:157], v[182:185], v[104:107]
	v_mfma_f32_16x16x32_bf16 v[96:99], v[166:169], v[182:185], v[96:99]
	v_mfma_f32_16x16x32_bf16 v[88:91], v[154:157], v[190:193], v[88:91]
	v_mfma_f32_16x16x32_bf16 v[80:83], v[166:169], v[190:193], v[80:83]
	v_mfma_f32_16x16x32_bf16 v[72:75], v[154:157], v[198:201], v[72:75]
	v_mfma_f32_16x16x32_bf16 v[64:67], v[166:169], v[198:201], v[64:67]
	v_mfma_f32_16x16x32_bf16 v[120:123], v[162:165], v[178:181], v[120:123]
	v_mfma_f32_16x16x32_bf16 v[112:115], v[170:173], v[178:181], v[112:115]
	v_mfma_f32_16x16x32_bf16 v[104:107], v[162:165], v[186:189], v[104:107]
	v_mfma_f32_16x16x32_bf16 v[96:99], v[170:173], v[186:189], v[96:99]
	v_mfma_f32_16x16x32_bf16 v[88:91], v[162:165], v[194:197], v[88:91]
	v_mfma_f32_16x16x32_bf16 v[80:83], v[170:173], v[194:197], v[80:83]
	v_mfma_f32_16x16x32_bf16 v[72:75], v[162:165], v[202:205], v[72:75]
	v_mfma_f32_16x16x32_bf16 v[64:67], v[170:173], v[202:205], v[64:67]
	s_setprio 0
	s_barrier
	s_add_i32 s83, s83, s31
	v_lshl_add_u64 v[132:133], s[86:87], 0, v[160:161]
	s_mov_b32 m0, s83
	ds_read_b128 v[174:177], v137 offset:16384
	ds_read_b128 v[178:181], v137 offset:17408
	ds_read_b128 v[182:185], v137 offset:18432
	ds_read_b128 v[186:189], v137 offset:19456
	ds_read_b128 v[190:193], v137 offset:20480
	ds_read_b128 v[194:197], v137 offset:21504
	ds_read_b128 v[198:201], v137 offset:22528
	ds_read_b128 v[202:205], v137 offset:23552
	global_load_lds_dwordx4 v[132:133], off
	v_lshl_add_u64 v[158:159], v[132:133], 0, s[14:15]
	s_add_i32 m0, s83, 0x2000
	s_add_i32 s83, s90, s31
	global_load_lds_dwordx4 v[158:159], off
	v_lshl_add_u64 v[158:159], v[132:133], 0, s[60:61]
	s_mov_b32 m0, s83
	s_nop 0
	global_load_lds_dwordx4 v[158:159], off
	v_lshl_add_u64 v[158:159], v[132:133], 0, s[52:53]
	s_add_i32 m0, s83, 0x2000
	s_nop 0
	global_load_lds_dwordx4 v[158:159], off
	v_lshl_add_u64 v[158:159], s[2:3], 0, v[128:129]
	s_mov_b32 m0, s33
	v_lshl_add_u64 v[206:207], v[158:159], 0, s[14:15]
	global_load_lds_dwordx4 v[158:159], off
	s_mov_b32 m0, s58
	s_nop 0
	global_load_lds_dwordx4 v[206:207], off
	s_waitcnt vmcnt(8)
	s_waitcnt lgkmcnt(0)
	s_barrier
	s_setprio 1
	v_mfma_f32_16x16x32_bf16 v[60:63], v[138:141], v[174:177], v[60:63]
	v_mfma_f32_16x16x32_bf16 v[52:55], v[146:149], v[174:177], v[52:55]
	v_mfma_f32_16x16x32_bf16 v[44:47], v[138:141], v[182:185], v[44:47]
	v_mfma_f32_16x16x32_bf16 v[36:39], v[146:149], v[182:185], v[36:39]
	v_mfma_f32_16x16x32_bf16 v[28:31], v[138:141], v[190:193], v[28:31]
	v_mfma_f32_16x16x32_bf16 v[20:23], v[146:149], v[190:193], v[20:23]
	v_mfma_f32_16x16x32_bf16 v[12:15], v[138:141], v[198:201], v[12:15]
	v_mfma_f32_16x16x32_bf16 v[4:7], v[146:149], v[198:201], v[4:7]
	v_mfma_f32_16x16x32_bf16 v[60:63], v[142:145], v[178:181], v[60:63]
	v_mfma_f32_16x16x32_bf16 v[52:55], v[150:153], v[178:181], v[52:55]
	v_mfma_f32_16x16x32_bf16 v[44:47], v[142:145], v[186:189], v[44:47]
	v_mfma_f32_16x16x32_bf16 v[36:39], v[150:153], v[186:189], v[36:39]
	v_mfma_f32_16x16x32_bf16 v[28:31], v[142:145], v[194:197], v[28:31]
	v_mfma_f32_16x16x32_bf16 v[20:23], v[150:153], v[194:197], v[20:23]
	v_mfma_f32_16x16x32_bf16 v[12:15], v[142:145], v[202:205], v[12:15]
	v_mfma_f32_16x16x32_bf16 v[4:7], v[150:153], v[202:205], v[4:7]
	v_mfma_f32_16x16x32_bf16 v[56:59], v[154:157], v[174:177], v[56:59]
	v_mfma_f32_16x16x32_bf16 v[48:51], v[166:169], v[174:177], v[48:51]
	v_mfma_f32_16x16x32_bf16 v[40:43], v[154:157], v[182:185], v[40:43]
	v_mfma_f32_16x16x32_bf16 v[32:35], v[166:169], v[182:185], v[32:35]
	v_mfma_f32_16x16x32_bf16 v[24:27], v[154:157], v[190:193], v[24:27]
	v_mfma_f32_16x16x32_bf16 v[16:19], v[166:169], v[190:193], v[16:19]
	v_mfma_f32_16x16x32_bf16 v[8:11], v[154:157], v[198:201], v[8:11]
	v_mfma_f32_16x16x32_bf16 v[0:3], v[166:169], v[198:201], v[0:3]
	v_mfma_f32_16x16x32_bf16 v[56:59], v[162:165], v[178:181], v[56:59]
	v_mfma_f32_16x16x32_bf16 v[48:51], v[170:173], v[178:181], v[48:51]
	v_mfma_f32_16x16x32_bf16 v[40:43], v[162:165], v[186:189], v[40:43]
	v_mfma_f32_16x16x32_bf16 v[32:35], v[170:173], v[186:189], v[32:35]
	v_mfma_f32_16x16x32_bf16 v[24:27], v[162:165], v[194:197], v[24:27]
	v_mfma_f32_16x16x32_bf16 v[16:19], v[170:173], v[194:197], v[16:19]
	v_mfma_f32_16x16x32_bf16 v[8:11], v[162:165], v[202:205], v[8:11]
	v_mfma_f32_16x16x32_bf16 v[0:3], v[170:173], v[202:205], v[0:3]
	s_setprio 0
	s_barrier
	s_add_i32 s2, 0, 0x18000
	s_add_i32 s3, 0, 0x1c000
	v_add_u32_e32 v150, s2, v135
	v_add_u32_e32 v170, s3, v135
	ds_read_b128 v[138:141], v150
	ds_read_b128 v[142:145], v150 offset:1024
	ds_read_b128 v[146:149], v150 offset:2048
	ds_read_b128 v[150:153], v150 offset:3072
	ds_read_b128 v[154:157], v170
	ds_read_b128 v[162:165], v170 offset:1024
	ds_read_b128 v[166:169], v170 offset:2048
	ds_read_b128 v[170:173], v170 offset:3072
	s_mov_b32 m0, s59
	v_lshl_add_u64 v[206:207], v[158:159], 0, s[60:61]
	ds_read_b128 v[174:177], v137 offset:32768
	ds_read_b128 v[178:181], v137 offset:33792
	ds_read_b128 v[182:185], v137 offset:34816
	ds_read_b128 v[186:189], v137 offset:35840
	ds_read_b128 v[190:193], v137 offset:36864
	ds_read_b128 v[194:197], v137 offset:37888
	ds_read_b128 v[198:201], v137 offset:38912
	ds_read_b128 v[202:205], v137 offset:39936
	global_load_lds_dwordx4 v[206:207], off
	v_lshl_add_u64 v[206:207], v[158:159], 0, s[52:53]
	s_mov_b32 m0, s63
	s_nop 0
	global_load_lds_dwordx4 v[206:207], off
	s_waitcnt vmcnt(8)
	s_waitcnt lgkmcnt(0)
	s_barrier
	s_setprio 1
	v_mfma_f32_16x16x32_bf16 v[124:127], v[138:141], v[174:177], v[124:127]
	v_mfma_f32_16x16x32_bf16 v[116:119], v[146:149], v[174:177], v[116:119]
	v_mfma_f32_16x16x32_bf16 v[108:111], v[138:141], v[182:185], v[108:111]
	v_mfma_f32_16x16x32_bf16 v[100:103], v[146:149], v[182:185], v[100:103]
	v_mfma_f32_16x16x32_bf16 v[92:95], v[138:141], v[190:193], v[92:95]
	v_mfma_f32_16x16x32_bf16 v[84:87], v[146:149], v[190:193], v[84:87]
	v_mfma_f32_16x16x32_bf16 v[76:79], v[138:141], v[198:201], v[76:79]
	v_mfma_f32_16x16x32_bf16 v[68:71], v[146:149], v[198:201], v[68:71]
	v_mfma_f32_16x16x32_bf16 v[124:127], v[142:145], v[178:181], v[124:127]
	v_mfma_f32_16x16x32_bf16 v[116:119], v[150:153], v[178:181], v[116:119]
	v_mfma_f32_16x16x32_bf16 v[108:111], v[142:145], v[186:189], v[108:111]
	v_mfma_f32_16x16x32_bf16 v[100:103], v[150:153], v[186:189], v[100:103]
	v_mfma_f32_16x16x32_bf16 v[92:95], v[142:145], v[194:197], v[92:95]
	v_mfma_f32_16x16x32_bf16 v[84:87], v[150:153], v[194:197], v[84:87]
	v_mfma_f32_16x16x32_bf16 v[76:79], v[142:145], v[202:205], v[76:79]
	v_mfma_f32_16x16x32_bf16 v[68:71], v[150:153], v[202:205], v[68:71]
	v_mfma_f32_16x16x32_bf16 v[120:123], v[154:157], v[174:177], v[120:123]
	v_mfma_f32_16x16x32_bf16 v[112:115], v[166:169], v[174:177], v[112:115]
	v_mfma_f32_16x16x32_bf16 v[104:107], v[154:157], v[182:185], v[104:107]
	v_mfma_f32_16x16x32_bf16 v[96:99], v[166:169], v[182:185], v[96:99]
	v_mfma_f32_16x16x32_bf16 v[88:91], v[154:157], v[190:193], v[88:91]
	v_mfma_f32_16x16x32_bf16 v[80:83], v[166:169], v[190:193], v[80:83]
	v_mfma_f32_16x16x32_bf16 v[72:75], v[154:157], v[198:201], v[72:75]
	v_mfma_f32_16x16x32_bf16 v[64:67], v[166:169], v[198:201], v[64:67]
	v_mfma_f32_16x16x32_bf16 v[120:123], v[162:165], v[178:181], v[120:123]
	v_mfma_f32_16x16x32_bf16 v[112:115], v[170:173], v[178:181], v[112:115]
	v_mfma_f32_16x16x32_bf16 v[104:107], v[162:165], v[186:189], v[104:107]
	v_mfma_f32_16x16x32_bf16 v[96:99], v[170:173], v[186:189], v[96:99]
	v_mfma_f32_16x16x32_bf16 v[88:91], v[162:165], v[194:197], v[88:91]
	v_mfma_f32_16x16x32_bf16 v[80:83], v[170:173], v[194:197], v[80:83]
	v_mfma_f32_16x16x32_bf16 v[72:75], v[162:165], v[202:205], v[72:75]
	v_mfma_f32_16x16x32_bf16 v[64:67], v[170:173], v[202:205], v[64:67]
	s_setprio 0
	s_barrier
	s_add_i32 s2, s2, s31
	v_lshl_add_u64 v[206:207], v[132:133], 0, s[56:57]
	s_mov_b32 m0, s2
	ds_read_b128 v[174:177], v137 offset:49152
	ds_read_b128 v[178:181], v137 offset:50176
	ds_read_b128 v[182:185], v137 offset:51200
	ds_read_b128 v[186:189], v137 offset:52224
	ds_read_b128 v[190:193], v137 offset:53248
	ds_read_b128 v[194:197], v137 offset:54272
	ds_read_b128 v[198:201], v137 offset:55296
	ds_read_b128 v[202:205], v137 offset:56320
	global_load_lds_dwordx4 v[206:207], off
	v_lshl_add_u64 v[206:207], v[132:133], 0, s[0:1]
	s_add_i32 m0, s2, 0x2000
	s_add_i32 s2, s3, s31
	global_load_lds_dwordx4 v[206:207], off
	v_lshl_add_u64 v[206:207], v[132:133], 0, s[24:25]
	s_mov_b32 m0, s2
	v_lshl_add_u64 v[132:133], v[132:133], 0, s[26:27]
	global_load_lds_dwordx4 v[206:207], off
	s_add_i32 m0, s2, 0x2000
	s_nop 0
	global_load_lds_dwordx4 v[132:133], off
	v_lshl_add_u64 v[132:133], v[158:159], 0, s[56:57]
	s_mov_b32 m0, s74
	s_nop 0
	global_load_lds_dwordx4 v[132:133], off
	v_lshl_add_u64 v[132:133], v[158:159], 0, s[0:1]
	s_mov_b32 m0, s75
	s_nop 0
	global_load_lds_dwordx4 v[132:133], off
	s_waitcnt vmcnt(8)
	s_waitcnt lgkmcnt(0)
	s_barrier
	s_setprio 1
	v_mfma_f32_16x16x32_bf16 v[60:63], v[138:141], v[174:177], v[60:63]
	v_mfma_f32_16x16x32_bf16 v[52:55], v[146:149], v[174:177], v[52:55]
	v_mfma_f32_16x16x32_bf16 v[44:47], v[138:141], v[182:185], v[44:47]
	v_mfma_f32_16x16x32_bf16 v[36:39], v[146:149], v[182:185], v[36:39]
	v_mfma_f32_16x16x32_bf16 v[28:31], v[138:141], v[190:193], v[28:31]
	v_mfma_f32_16x16x32_bf16 v[20:23], v[146:149], v[190:193], v[20:23]
	v_mfma_f32_16x16x32_bf16 v[12:15], v[138:141], v[198:201], v[12:15]
	v_mfma_f32_16x16x32_bf16 v[4:7], v[146:149], v[198:201], v[4:7]
	v_mfma_f32_16x16x32_bf16 v[60:63], v[142:145], v[178:181], v[60:63]
	v_mfma_f32_16x16x32_bf16 v[52:55], v[150:153], v[178:181], v[52:55]
	v_mfma_f32_16x16x32_bf16 v[44:47], v[142:145], v[186:189], v[44:47]
	v_mfma_f32_16x16x32_bf16 v[36:39], v[150:153], v[186:189], v[36:39]
	v_mfma_f32_16x16x32_bf16 v[28:31], v[142:145], v[194:197], v[28:31]
	v_mfma_f32_16x16x32_bf16 v[20:23], v[150:153], v[194:197], v[20:23]
	v_mfma_f32_16x16x32_bf16 v[12:15], v[142:145], v[202:205], v[12:15]
	v_mfma_f32_16x16x32_bf16 v[4:7], v[150:153], v[202:205], v[4:7]
	v_mfma_f32_16x16x32_bf16 v[56:59], v[154:157], v[174:177], v[56:59]
	v_mfma_f32_16x16x32_bf16 v[48:51], v[166:169], v[174:177], v[48:51]
	v_mfma_f32_16x16x32_bf16 v[40:43], v[154:157], v[182:185], v[40:43]
	v_mfma_f32_16x16x32_bf16 v[32:35], v[166:169], v[182:185], v[32:35]
	v_mfma_f32_16x16x32_bf16 v[24:27], v[154:157], v[190:193], v[24:27]
	v_mfma_f32_16x16x32_bf16 v[16:19], v[166:169], v[190:193], v[16:19]
	v_mfma_f32_16x16x32_bf16 v[8:11], v[154:157], v[198:201], v[8:11]
	v_mfma_f32_16x16x32_bf16 v[0:3], v[166:169], v[198:201], v[0:3]
	v_mfma_f32_16x16x32_bf16 v[56:59], v[162:165], v[178:181], v[56:59]
	v_mfma_f32_16x16x32_bf16 v[48:51], v[170:173], v[178:181], v[48:51]
	v_mfma_f32_16x16x32_bf16 v[40:43], v[162:165], v[186:189], v[40:43]
	v_mfma_f32_16x16x32_bf16 v[32:35], v[170:173], v[186:189], v[32:35]
	v_mfma_f32_16x16x32_bf16 v[24:27], v[162:165], v[194:197], v[24:27]
	v_mfma_f32_16x16x32_bf16 v[16:19], v[170:173], v[194:197], v[16:19]
	v_mfma_f32_16x16x32_bf16 v[8:11], v[162:165], v[202:205], v[8:11]
	v_mfma_f32_16x16x32_bf16 v[0:3], v[170:173], v[202:205], v[0:3]
	s_setprio 0
	s_barrier
	s_add_u32 s54, s54, 0x100
	s_addc_u32 s55, s55, 0
	s_add_u32 s22, s22, 0x100
	s_addc_u32 s23, s23, 0
	s_cmp_ge_i32 s81, s77
	s_mov_b32 s2, s81
	s_cbranch_scc0 .LBB0_1232

.LBB0_1311:
	s_add_i32 s77, s2, 2
	s_add_u32 s78, s46, 0xfff20080
	s_addc_u32 s3, s47, -1
	s_cmp_eq_u32 s58, s2
	s_cselect_b32 s3, s19, s3
	s_cselect_b32 s2, s18, s78
	s_cselect_b32 s79, s39, s23
	s_cselect_b32 s78, s38, s22
	s_add_i32 s80, 0, 0x10000
	s_add_i32 s81, 0, 0x14000
	v_add_u32_e32 v142, s80, v153
	v_add_u32_e32 v150, s81, v153
	ds_read_b128 v[130:133], v142
	ds_read_b128 v[134:137], v142 offset:1024
	ds_read_b128 v[138:141], v142 offset:2048
	ds_read_b128 v[142:145], v142 offset:3072
	ds_read_b128 v[146:149], v150
	ds_read_b128 v[156:159], v150 offset:1024
	ds_read_b128 v[162:165], v150 offset:2048
	ds_read_b128 v[166:169], v150 offset:3072
	v_lshl_add_u64 v[150:151], s[46:47], 0, v[128:129]
	s_add_i32 m0, s33, 0xc000
	ds_read_b128 v[170:173], v155
	ds_read_b128 v[174:177], v155 offset:1024
	ds_read_b128 v[178:181], v155 offset:2048
	ds_read_b128 v[182:185], v155 offset:3072
	ds_read_b128 v[186:189], v155 offset:4096
	ds_read_b128 v[190:193], v155 offset:5120
	ds_read_b128 v[194:197], v155 offset:6144
	ds_read_b128 v[198:201], v155 offset:7168
	global_load_lds_dwordx4 v[150:151], off
	v_lshl_add_u64 v[150:151], v[150:151], 0, s[84:85]
	s_add_i32 m0, s33, 0xe000
	s_nop 0
	global_load_lds_dwordx4 v[150:151], off
	s_waitcnt vmcnt(8)
	s_waitcnt lgkmcnt(0)
	s_barrier
	s_setprio 1
	v_mfma_f32_16x16x32_bf16 v[124:127], v[130:133], v[170:173], v[124:127]
	v_mfma_f32_16x16x32_bf16 v[120:123], v[138:141], v[170:173], v[120:123]
	v_mfma_f32_16x16x32_bf16 v[108:111], v[130:133], v[178:181], v[108:111]
	v_mfma_f32_16x16x32_bf16 v[104:107], v[138:141], v[178:181], v[104:107]
	v_mfma_f32_16x16x32_bf16 v[92:95], v[130:133], v[186:189], v[92:95]
	v_mfma_f32_16x16x32_bf16 v[88:91], v[138:141], v[186:189], v[88:91]
	v_mfma_f32_16x16x32_bf16 v[76:79], v[130:133], v[194:197], v[76:79]
	v_mfma_f32_16x16x32_bf16 v[72:75], v[138:141], v[194:197], v[72:75]
	v_mfma_f32_16x16x32_bf16 v[124:127], v[134:137], v[174:177], v[124:127]
	v_mfma_f32_16x16x32_bf16 v[120:123], v[142:145], v[174:177], v[120:123]
	v_mfma_f32_16x16x32_bf16 v[108:111], v[134:137], v[182:185], v[108:111]
	v_mfma_f32_16x16x32_bf16 v[104:107], v[142:145], v[182:185], v[104:107]
	v_mfma_f32_16x16x32_bf16 v[92:95], v[134:137], v[190:193], v[92:95]
	v_mfma_f32_16x16x32_bf16 v[88:91], v[142:145], v[190:193], v[88:91]
	v_mfma_f32_16x16x32_bf16 v[76:79], v[134:137], v[198:201], v[76:79]
	v_mfma_f32_16x16x32_bf16 v[72:75], v[142:145], v[198:201], v[72:75]
	v_mfma_f32_16x16x32_bf16 v[116:119], v[146:149], v[170:173], v[116:119]
	v_mfma_f32_16x16x32_bf16 v[112:115], v[162:165], v[170:173], v[112:115]
	v_mfma_f32_16x16x32_bf16 v[100:103], v[146:149], v[178:181], v[100:103]
	v_mfma_f32_16x16x32_bf16 v[96:99], v[162:165], v[178:181], v[96:99]
	v_mfma_f32_16x16x32_bf16 v[84:87], v[146:149], v[186:189], v[84:87]
	v_mfma_f32_16x16x32_bf16 v[80:83], v[162:165], v[186:189], v[80:83]
	v_mfma_f32_16x16x32_bf16 v[68:71], v[146:149], v[194:197], v[68:71]
	v_mfma_f32_16x16x32_bf16 v[64:67], v[162:165], v[194:197], v[64:67]
	v_mfma_f32_16x16x32_bf16 v[116:119], v[156:159], v[174:177], v[116:119]
	v_mfma_f32_16x16x32_bf16 v[112:115], v[166:169], v[174:177], v[112:115]
	v_mfma_f32_16x16x32_bf16 v[100:103], v[156:159], v[182:185], v[100:103]
	v_mfma_f32_16x16x32_bf16 v[96:99], v[166:169], v[182:185], v[96:99]
	v_mfma_f32_16x16x32_bf16 v[84:87], v[156:159], v[190:193], v[84:87]
	v_mfma_f32_16x16x32_bf16 v[80:83], v[166:169], v[190:193], v[80:83]
	v_mfma_f32_16x16x32_bf16 v[68:71], v[156:159], v[198:201], v[68:71]
	v_mfma_f32_16x16x32_bf16 v[64:67], v[166:169], v[198:201], v[64:67]
	s_setprio 0
	s_barrier
	v_lshl_add_u64 v[150:151], s[78:79], 0, v[160:161]
	s_add_i32 s78, s80, s31
	s_mov_b32 m0, s78
	ds_read_b128 v[170:173], v155 offset:16384
	ds_read_b128 v[174:177], v155 offset:17408
	ds_read_b128 v[178:181], v155 offset:18432
	ds_read_b128 v[182:185], v155 offset:19456
	ds_read_b128 v[186:189], v155 offset:20480
	ds_read_b128 v[190:193], v155 offset:21504
	ds_read_b128 v[194:197], v155 offset:22528
	ds_read_b128 v[198:201], v155 offset:23552
	global_load_lds_dwordx4 v[150:151], off
	v_lshl_add_u64 v[202:203], v[150:151], 0, s[84:85]
	s_add_i32 m0, s78, 0x2000
	s_add_i32 s78, s81, s31
	global_load_lds_dwordx4 v[202:203], off
	v_lshl_add_u64 v[202:203], v[150:151], 0, s[4:5]
	s_mov_b32 m0, s78
	s_nop 0
	global_load_lds_dwordx4 v[202:203], off
	v_lshl_add_u64 v[202:203], v[150:151], 0, s[12:13]
	s_add_i32 m0, s78, 0x2000
	s_nop 0
	global_load_lds_dwordx4 v[202:203], off
	v_lshl_add_u64 v[202:203], s[2:3], 0, v[160:161]
	s_mov_b32 m0, s33
	v_lshl_add_u64 v[204:205], v[202:203], 0, s[84:85]
	global_load_lds_dwordx4 v[202:203], off
	s_mov_b32 m0, s48
	s_nop 0
	global_load_lds_dwordx4 v[204:205], off
	s_waitcnt vmcnt(8)
	s_waitcnt lgkmcnt(0)
	s_barrier
	s_setprio 1
	v_mfma_f32_16x16x32_bf16 v[60:63], v[130:133], v[170:173], v[60:63]
	v_mfma_f32_16x16x32_bf16 v[56:59], v[138:141], v[170:173], v[56:59]
	v_mfma_f32_16x16x32_bf16 v[44:47], v[130:133], v[178:181], v[44:47]
	v_mfma_f32_16x16x32_bf16 v[40:43], v[138:141], v[178:181], v[40:43]
	v_mfma_f32_16x16x32_bf16 v[28:31], v[130:133], v[186:189], v[28:31]
	v_mfma_f32_16x16x32_bf16 v[24:27], v[138:141], v[186:189], v[24:27]
	v_mfma_f32_16x16x32_bf16 v[12:15], v[130:133], v[194:197], v[12:15]
	v_mfma_f32_16x16x32_bf16 v[8:11], v[138:141], v[194:197], v[8:11]
	v_mfma_f32_16x16x32_bf16 v[60:63], v[134:137], v[174:177], v[60:63]
	v_mfma_f32_16x16x32_bf16 v[56:59], v[142:145], v[174:177], v[56:59]
	v_mfma_f32_16x16x32_bf16 v[44:47], v[134:137], v[182:185], v[44:47]
	v_mfma_f32_16x16x32_bf16 v[40:43], v[142:145], v[182:185], v[40:43]
	v_mfma_f32_16x16x32_bf16 v[28:31], v[134:137], v[190:193], v[28:31]
	v_mfma_f32_16x16x32_bf16 v[24:27], v[142:145], v[190:193], v[24:27]
	v_mfma_f32_16x16x32_bf16 v[12:15], v[134:137], v[198:201], v[12:15]
	v_mfma_f32_16x16x32_bf16 v[8:11], v[142:145], v[198:201], v[8:11]
	v_mfma_f32_16x16x32_bf16 v[52:55], v[146:149], v[170:173], v[52:55]
	v_mfma_f32_16x16x32_bf16 v[48:51], v[162:165], v[170:173], v[48:51]
	v_mfma_f32_16x16x32_bf16 v[36:39], v[146:149], v[178:181], v[36:39]
	v_mfma_f32_16x16x32_bf16 v[32:35], v[162:165], v[178:181], v[32:35]
	v_mfma_f32_16x16x32_bf16 v[20:23], v[146:149], v[186:189], v[20:23]
	v_mfma_f32_16x16x32_bf16 v[16:19], v[162:165], v[186:189], v[16:19]
	v_mfma_f32_16x16x32_bf16 v[4:7], v[146:149], v[194:197], v[4:7]
	v_mfma_f32_16x16x32_bf16 v[0:3], v[162:165], v[194:197], v[0:3]
	v_mfma_f32_16x16x32_bf16 v[52:55], v[156:159], v[174:177], v[52:55]
	v_mfma_f32_16x16x32_bf16 v[48:51], v[166:169], v[174:177], v[48:51]
	v_mfma_f32_16x16x32_bf16 v[36:39], v[156:159], v[182:185], v[36:39]
	v_mfma_f32_16x16x32_bf16 v[32:35], v[166:169], v[182:185], v[32:35]
	v_mfma_f32_16x16x32_bf16 v[20:23], v[156:159], v[190:193], v[20:23]
	v_mfma_f32_16x16x32_bf16 v[16:19], v[166:169], v[190:193], v[16:19]
	v_mfma_f32_16x16x32_bf16 v[4:7], v[156:159], v[198:201], v[4:7]
	v_mfma_f32_16x16x32_bf16 v[0:3], v[166:169], v[198:201], v[0:3]
	s_setprio 0
	s_barrier
	s_add_i32 s2, 0, 0x18000
	s_add_i32 s3, 0, 0x1c000
	v_add_u32_e32 v142, s2, v153
	v_add_u32_e32 v166, s3, v153
	ds_read_b128 v[130:133], v142
	ds_read_b128 v[134:137], v142 offset:1024
	ds_read_b128 v[138:141], v142 offset:2048
	ds_read_b128 v[142:145], v142 offset:3072
	ds_read_b128 v[146:149], v166
	ds_read_b128 v[156:159], v166 offset:1024
	ds_read_b128 v[162:165], v166 offset:2048
	ds_read_b128 v[166:169], v166 offset:3072
	s_mov_b32 m0, s49
	v_lshl_add_u64 v[204:205], v[202:203], 0, s[4:5]
	ds_read_b128 v[170:173], v155 offset:32768
	ds_read_b128 v[174:177], v155 offset:33792
	ds_read_b128 v[178:181], v155 offset:34816
	ds_read_b128 v[182:185], v155 offset:35840
	ds_read_b128 v[186:189], v155 offset:36864
	ds_read_b128 v[190:193], v155 offset:37888
	ds_read_b128 v[194:197], v155 offset:38912
	ds_read_b128 v[198:201], v155 offset:39936
	global_load_lds_dwordx4 v[204:205], off
	v_lshl_add_u64 v[204:205], v[202:203], 0, s[12:13]
	s_mov_b32 m0, s50
	s_nop 0
	global_load_lds_dwordx4 v[204:205], off
	s_waitcnt vmcnt(8)
	s_waitcnt lgkmcnt(0)
	s_barrier
	s_setprio 1
	v_mfma_f32_16x16x32_bf16 v[124:127], v[130:133], v[170:173], v[124:127]
	v_mfma_f32_16x16x32_bf16 v[120:123], v[138:141], v[170:173], v[120:123]
	v_mfma_f32_16x16x32_bf16 v[108:111], v[130:133], v[178:181], v[108:111]
	v_mfma_f32_16x16x32_bf16 v[104:107], v[138:141], v[178:181], v[104:107]
	v_mfma_f32_16x16x32_bf16 v[92:95], v[130:133], v[186:189], v[92:95]
	v_mfma_f32_16x16x32_bf16 v[88:91], v[138:141], v[186:189], v[88:91]
	v_mfma_f32_16x16x32_bf16 v[76:79], v[130:133], v[194:197], v[76:79]
	v_mfma_f32_16x16x32_bf16 v[72:75], v[138:141], v[194:197], v[72:75]
	v_mfma_f32_16x16x32_bf16 v[124:127], v[134:137], v[174:177], v[124:127]
	v_mfma_f32_16x16x32_bf16 v[120:123], v[142:145], v[174:177], v[120:123]
	v_mfma_f32_16x16x32_bf16 v[108:111], v[134:137], v[182:185], v[108:111]
	v_mfma_f32_16x16x32_bf16 v[104:107], v[142:145], v[182:185], v[104:107]
	v_mfma_f32_16x16x32_bf16 v[92:95], v[134:137], v[190:193], v[92:95]
	v_mfma_f32_16x16x32_bf16 v[88:91], v[142:145], v[190:193], v[88:91]
	v_mfma_f32_16x16x32_bf16 v[76:79], v[134:137], v[198:201], v[76:79]
	v_mfma_f32_16x16x32_bf16 v[72:75], v[142:145], v[198:201], v[72:75]
	v_mfma_f32_16x16x32_bf16 v[116:119], v[146:149], v[170:173], v[116:119]
	v_mfma_f32_16x16x32_bf16 v[112:115], v[162:165], v[170:173], v[112:115]
	v_mfma_f32_16x16x32_bf16 v[100:103], v[146:149], v[178:181], v[100:103]
	v_mfma_f32_16x16x32_bf16 v[96:99], v[162:165], v[178:181], v[96:99]
	v_mfma_f32_16x16x32_bf16 v[84:87], v[146:149], v[186:189], v[84:87]
	v_mfma_f32_16x16x32_bf16 v[80:83], v[162:165], v[186:189], v[80:83]
	v_mfma_f32_16x16x32_bf16 v[68:71], v[146:149], v[194:197], v[68:71]
	v_mfma_f32_16x16x32_bf16 v[64:67], v[162:165], v[194:197], v[64:67]
	v_mfma_f32_16x16x32_bf16 v[116:119], v[156:159], v[174:177], v[116:119]
	v_mfma_f32_16x16x32_bf16 v[112:115], v[166:169], v[174:177], v[112:115]
	v_mfma_f32_16x16x32_bf16 v[100:103], v[156:159], v[182:185], v[100:103]
	v_mfma_f32_16x16x32_bf16 v[96:99], v[166:169], v[182:185], v[96:99]
	v_mfma_f32_16x16x32_bf16 v[84:87], v[156:159], v[190:193], v[84:87]
	v_mfma_f32_16x16x32_bf16 v[80:83], v[166:169], v[190:193], v[80:83]
	v_mfma_f32_16x16x32_bf16 v[68:71], v[156:159], v[198:201], v[68:71]
	v_mfma_f32_16x16x32_bf16 v[64:67], v[166:169], v[198:201], v[64:67]
	s_setprio 0
	s_barrier
	s_add_i32 s2, s2, s31
	v_lshl_add_u64 v[204:205], v[150:151], 0, s[56:57]
	s_mov_b32 m0, s2
	ds_read_b128 v[170:173], v155 offset:49152
	ds_read_b128 v[174:177], v155 offset:50176
	ds_read_b128 v[178:181], v155 offset:51200
	ds_read_b128 v[182:185], v155 offset:52224
	ds_read_b128 v[186:189], v155 offset:53248
	ds_read_b128 v[190:193], v155 offset:54272
	ds_read_b128 v[194:197], v155 offset:55296
	ds_read_b128 v[198:201], v155 offset:56320
	global_load_lds_dwordx4 v[204:205], off
	v_lshl_add_u64 v[204:205], v[150:151], 0, s[64:65]
	s_add_i32 m0, s2, 0x2000
	s_add_i32 s2, s3, s31
	global_load_lds_dwordx4 v[204:205], off
	v_lshl_add_u64 v[204:205], v[150:151], 0, s[72:73]
	s_mov_b32 m0, s2
	v_lshl_add_u64 v[150:151], v[150:151], 0, s[86:87]
	global_load_lds_dwordx4 v[204:205], off
	s_add_i32 m0, s2, 0x2000
	s_nop 0
	global_load_lds_dwordx4 v[150:151], off
	v_lshl_add_u64 v[150:151], v[202:203], 0, s[56:57]
	s_mov_b32 m0, s51
	s_nop 0
	global_load_lds_dwordx4 v[150:151], off
	v_lshl_add_u64 v[150:151], v[202:203], 0, s[64:65]
	s_mov_b32 m0, s54
	s_nop 0
	global_load_lds_dwordx4 v[150:151], off
	s_waitcnt vmcnt(8)
	s_waitcnt lgkmcnt(0)
	s_barrier
	s_setprio 1
	v_mfma_f32_16x16x32_bf16 v[60:63], v[130:133], v[170:173], v[60:63]
	v_mfma_f32_16x16x32_bf16 v[56:59], v[138:141], v[170:173], v[56:59]
	v_mfma_f32_16x16x32_bf16 v[44:47], v[130:133], v[178:181], v[44:47]
	v_mfma_f32_16x16x32_bf16 v[40:43], v[138:141], v[178:181], v[40:43]
	v_mfma_f32_16x16x32_bf16 v[28:31], v[130:133], v[186:189], v[28:31]
	v_mfma_f32_16x16x32_bf16 v[24:27], v[138:141], v[186:189], v[24:27]
	v_mfma_f32_16x16x32_bf16 v[12:15], v[130:133], v[194:197], v[12:15]
	v_mfma_f32_16x16x32_bf16 v[8:11], v[138:141], v[194:197], v[8:11]
	v_mfma_f32_16x16x32_bf16 v[60:63], v[134:137], v[174:177], v[60:63]
	v_mfma_f32_16x16x32_bf16 v[56:59], v[142:145], v[174:177], v[56:59]
	v_mfma_f32_16x16x32_bf16 v[44:47], v[134:137], v[182:185], v[44:47]
	v_mfma_f32_16x16x32_bf16 v[40:43], v[142:145], v[182:185], v[40:43]
	v_mfma_f32_16x16x32_bf16 v[28:31], v[134:137], v[190:193], v[28:31]
	v_mfma_f32_16x16x32_bf16 v[24:27], v[142:145], v[190:193], v[24:27]
	v_mfma_f32_16x16x32_bf16 v[12:15], v[134:137], v[198:201], v[12:15]
	v_mfma_f32_16x16x32_bf16 v[8:11], v[142:145], v[198:201], v[8:11]
	v_mfma_f32_16x16x32_bf16 v[52:55], v[146:149], v[170:173], v[52:55]
	v_mfma_f32_16x16x32_bf16 v[48:51], v[162:165], v[170:173], v[48:51]
	v_mfma_f32_16x16x32_bf16 v[36:39], v[146:149], v[178:181], v[36:39]
	v_mfma_f32_16x16x32_bf16 v[32:35], v[162:165], v[178:181], v[32:35]
	v_mfma_f32_16x16x32_bf16 v[20:23], v[146:149], v[186:189], v[20:23]
	v_mfma_f32_16x16x32_bf16 v[16:19], v[162:165], v[186:189], v[16:19]
	v_mfma_f32_16x16x32_bf16 v[4:7], v[146:149], v[194:197], v[4:7]
	v_mfma_f32_16x16x32_bf16 v[0:3], v[162:165], v[194:197], v[0:3]
	v_mfma_f32_16x16x32_bf16 v[52:55], v[156:159], v[174:177], v[52:55]
	v_mfma_f32_16x16x32_bf16 v[48:51], v[166:169], v[174:177], v[48:51]
	v_mfma_f32_16x16x32_bf16 v[36:39], v[156:159], v[182:185], v[36:39]
	v_mfma_f32_16x16x32_bf16 v[32:35], v[166:169], v[182:185], v[32:35]
	v_mfma_f32_16x16x32_bf16 v[20:23], v[156:159], v[190:193], v[20:23]
	v_mfma_f32_16x16x32_bf16 v[16:19], v[166:169], v[190:193], v[16:19]
	v_mfma_f32_16x16x32_bf16 v[4:7], v[156:159], v[198:201], v[4:7]
	v_mfma_f32_16x16x32_bf16 v[0:3], v[166:169], v[198:201], v[0:3]
	s_setprio 0
	s_barrier
	s_add_u32 s46, s46, 0x100
	s_addc_u32 s47, s47, 0
	s_add_u32 s22, s22, 0x100
	s_addc_u32 s23, s23, 0
	s_cmp_ge_i32 s77, s55
	s_mov_b32 s2, s77
	s_cbranch_scc0 .LBB0_1311
